# baseline (speedup 1.0000x reference)
_Z7gemm128ILi2ELi128EEv8GemmArgs:
	s_cmp_ge_u32 s2, 0x100
	s_cbranch_scc1 .Lup_exit
	s_load_dwordx4 s[4:7], s[0:1], 0x0
	s_load_dwordx2 s[8:9], s[0:1], 0x20
	s_load_dwordx2 s[10:11], s[0:1], 0x48
	s_and_b32 s12, s2, 7
	s_lshr_b32 s13, s2, 3
	s_lshl_b32 s12, s12, 5
	s_add_u32 s12, s12, s13
	s_and_b32 s13, s12, 3
	s_lshr_b32 s12, s12, 2
	s_lshl_b32 s12, s12, 7
	s_lshl_b32 s13, s13, 8
	s_add_u32 s13, s13, 0x800
	s_mov_b32 s24, 0xc0135761
	s_mov_b32 s26, 0x3dd2d3e8
	s_mov_b32 s27, 0x3dd2d3e8
	s_mov_b32 s28, 0xc0135761
	s_mov_b32 s29, 0xc0135761
	s_mov_b32 s30, 1.0
	s_mov_b32 s31, 1.0
	v_lshrrev_b32_e32 v1, 6, v0
	v_and_b32_e32 v24, 7, v0
	v_bfe_u32 v25, v0, 4, 3
	v_xor_b32_e32 v24, v24, v25
	v_readfirstlane_b32 s14, v1
	v_lshrrev_b32_e32 v25, 3, v0
	v_mul_u32_u24_e32 v25, 0x600, v25
	v_lshl_add_u32 v2, v24, 4, v25
	s_mov_b32 s22, 0xc000
	v_add_u32_e32 v3, s22, v2
	v_add_u32_e32 v4, s22, v3
	v_add_u32_e32 v5, s22, v4
	v_add_u32_e32 v6, s22, v5
	v_add_u32_e32 v7, s22, v6
	v_add_u32_e32 v8, s22, v7
	v_add_u32_e32 v9, s22, v8
	v_and_b32_e32 v24, 15, v0
	v_bfe_u32 v25, v0, 4, 2
	v_lshrrev_b32_e32 v26, 1, v24
	v_xor_b32_e32 v26, v26, v25
	v_lshlrev_b32_e32 v26, 4, v26
	v_bfe_u32 v27, v0, 7, 1
	v_bfe_u32 v28, v0, 6, 1
	v_lshl_add_u32 v29, v27, 6, v24
	v_lshl_add_u32 v10, v29, 7, v26
	v_lshl_add_u32 v30, v28, 7, v24
	v_lshl_add_u32 v11, v30, 7, v26
	v_add_u32_e32 v11, 0x4000, v11
	v_add_u32_e32 v29, s12, v29
	v_lshlrev_b32_e32 v21, 6, v29
	v_mul_u32_u24_e32 v29, 0x1800, v29
	v_lshlrev_b32_e32 v30, 7, v28
	v_lshl_add_u32 v30, v25, 2, v30
	v_add_u32_e32 v30, s13, v30
	v_lshl_add_u32 v16, v30, 1, v29
	s_mov_b32 s22, 0x18000
	v_add_u32_e32 v17, s22, v16
	v_add_u32_e32 v18, s22, v17
	v_add_u32_e32 v19, s22, v18
	s_waitcnt lgkmcnt(0)
	s_mul_i32 s22, s12, 0x600
	s_add_u32 s16, s4, s22
	s_addc_u32 s17, s5, 0
	s_mul_i32 s22, s13, 0x600
	s_add_u32 s18, s6, s22
	s_addc_u32 s19, s7, 0
	s_lshl_b32 s20, s14, 10
	s_mov_b32 s21, 0
	global_load_dwordx4 v[128:131], v21, s[8:9] offset:0
	global_load_dwordx4 v[132:135], v21, s[8:9] offset:16
	global_load_dwordx4 v[136:139], v21, s[8:9] offset:32
	global_load_dwordx4 v[140:143], v21, s[8:9] offset:48
	global_load_dwordx4 v[144:147], v21, s[8:9] offset:1024
	global_load_dwordx4 v[148:151], v21, s[8:9] offset:1040
	global_load_dwordx4 v[152:155], v21, s[8:9] offset:1056
	global_load_dwordx4 v[156:159], v21, s[8:9] offset:1072
	global_load_dwordx4 v[160:163], v21, s[8:9] offset:2048
	global_load_dwordx4 v[164:167], v21, s[8:9] offset:2064
	global_load_dwordx4 v[168:171], v21, s[8:9] offset:2080
	global_load_dwordx4 v[172:175], v21, s[8:9] offset:2096
	global_load_dwordx4 v[176:179], v21, s[8:9] offset:3072
	global_load_dwordx4 v[180:183], v21, s[8:9] offset:3088
	global_load_dwordx4 v[184:187], v21, s[8:9] offset:3104
	global_load_dwordx4 v[188:191], v21, s[8:9] offset:3120
	v_mov_b32_e32 v31, 0x358637bd
	s_add_u32 m0, s20, 0x0
	s_nop 0
	global_load_lds_dwordx4 v2, s[16:17]
	s_add_u32 m0, s20, 0x1000
	s_nop 0
	global_load_lds_dwordx4 v3, s[16:17]
	s_add_u32 m0, s20, 0x2000
	s_nop 0
	global_load_lds_dwordx4 v4, s[16:17]
	s_add_u32 m0, s20, 0x3000
	s_nop 0
	global_load_lds_dwordx4 v5, s[16:17]
	s_add_u32 m0, s20, 0x4000
	s_nop 0
	global_load_lds_dwordx4 v2, s[18:19]
	s_add_u32 m0, s20, 0x5000
	s_nop 0
	global_load_lds_dwordx4 v3, s[18:19]
	s_add_u32 m0, s20, 0x6000
	s_nop 0
	global_load_lds_dwordx4 v4, s[18:19]
	s_add_u32 m0, s20, 0x7000
	s_nop 0
	global_load_lds_dwordx4 v5, s[18:19]
	s_add_u32 m0, s20, 0x8000
	s_nop 0
	global_load_lds_dwordx4 v6, s[18:19]
	s_add_u32 m0, s20, 0x9000
	s_nop 0
	global_load_lds_dwordx4 v7, s[18:19]
	s_add_u32 m0, s20, 0xa000
	s_nop 0
	global_load_lds_dwordx4 v8, s[18:19]
	s_add_u32 m0, s20, 0xb000
	s_nop 0
	global_load_lds_dwordx4 v9, s[18:19]
	s_add_u32 s16, s16, 0x80
	s_addc_u32 s17, s17, 0
	s_add_u32 s18, s18, 0x80
	s_addc_u32 s19, s19, 0
	s_add_u32 s20, s20, 0xc000
	s_sub_u32 s22, s20, 0x24000
	s_cmp_ge_u32 s20, 0x24000
	s_cselect_b32 s20, s22, s20
	s_add_u32 m0, s20, 0x0
	s_nop 0
	global_load_lds_dwordx4 v2, s[16:17]
	s_add_u32 m0, s20, 0x1000
	s_nop 0
	global_load_lds_dwordx4 v3, s[16:17]
	s_add_u32 m0, s20, 0x2000
	s_nop 0
	global_load_lds_dwordx4 v4, s[16:17]
	s_add_u32 m0, s20, 0x3000
	s_nop 0
	global_load_lds_dwordx4 v5, s[16:17]
	s_add_u32 m0, s20, 0x4000
	s_nop 0
	global_load_lds_dwordx4 v2, s[18:19]
	s_add_u32 m0, s20, 0x5000
	s_nop 0
	global_load_lds_dwordx4 v3, s[18:19]
	s_add_u32 m0, s20, 0x6000
	s_nop 0
	global_load_lds_dwordx4 v4, s[18:19]
	s_add_u32 m0, s20, 0x7000
	s_nop 0
	global_load_lds_dwordx4 v5, s[18:19]
	s_add_u32 m0, s20, 0x8000
	s_nop 0
	global_load_lds_dwordx4 v6, s[18:19]
	s_add_u32 m0, s20, 0x9000
	s_nop 0
	global_load_lds_dwordx4 v7, s[18:19]
	s_add_u32 m0, s20, 0xa000
	s_nop 0
	global_load_lds_dwordx4 v8, s[18:19]
	s_add_u32 m0, s20, 0xb000
	s_nop 0
	global_load_lds_dwordx4 v9, s[18:19]
	s_add_u32 s16, s16, 0x80
	s_addc_u32 s17, s17, 0
	s_add_u32 s18, s18, 0x80
	s_addc_u32 s19, s19, 0
	s_add_u32 s20, s20, 0xc000
	s_sub_u32 s22, s20, 0x24000
	s_cmp_ge_u32 s20, 0x24000
	s_cselect_b32 s20, s22, s20
	s_add_u32 m0, s20, 0x0
	s_nop 0
	global_load_lds_dwordx4 v2, s[16:17]
	s_add_u32 m0, s20, 0x1000
	s_nop 0
	global_load_lds_dwordx4 v3, s[16:17]
	s_add_u32 m0, s20, 0x2000
	s_nop 0
	global_load_lds_dwordx4 v4, s[16:17]
	s_add_u32 m0, s20, 0x3000
	s_nop 0
	global_load_lds_dwordx4 v5, s[16:17]
	s_add_u32 m0, s20, 0x4000
	s_nop 0
	global_load_lds_dwordx4 v2, s[18:19]
	s_add_u32 m0, s20, 0x5000
	s_nop 0
	global_load_lds_dwordx4 v3, s[18:19]
	s_waitcnt vmcnt(30)
	v_add_f32_e32 v128, v128, v129
	v_add_f32_e32 v130, v130, v131
	v_add_f32_e32 v132, v132, v133
	v_add_f32_e32 v134, v134, v135
	v_add_f32_e32 v136, v136, v137
	v_add_f32_e32 v138, v138, v139
	v_add_f32_e32 v140, v140, v141
	v_add_f32_e32 v142, v142, v143
	v_add_f32_e32 v128, v128, v130
	v_add_f32_e32 v132, v132, v134
	v_add_f32_e32 v136, v136, v138
	v_add_f32_e32 v140, v140, v142
	v_add_f32_e32 v128, v128, v132
	v_add_f32_e32 v136, v136, v140
	v_add_f32_e32 v128, v128, v136
	v_add_f32_e32 v144, v144, v145
	v_add_f32_e32 v146, v146, v147
	v_add_f32_e32 v148, v148, v149
	v_add_f32_e32 v150, v150, v151
	v_add_f32_e32 v152, v152, v153
	v_add_f32_e32 v154, v154, v155
	v_add_f32_e32 v156, v156, v157
	v_add_f32_e32 v158, v158, v159
	v_add_f32_e32 v144, v144, v146
	v_add_f32_e32 v148, v148, v150
	v_add_f32_e32 v152, v152, v154
	v_add_f32_e32 v156, v156, v158
	v_add_f32_e32 v144, v144, v148
	v_add_f32_e32 v152, v152, v156
	v_add_f32_e32 v144, v144, v152
	v_add_f32_e32 v160, v160, v161
	v_add_f32_e32 v162, v162, v163
	v_add_f32_e32 v164, v164, v165
	v_add_f32_e32 v166, v166, v167
	v_add_f32_e32 v168, v168, v169
	v_add_f32_e32 v170, v170, v171
	v_add_f32_e32 v172, v172, v173
	v_add_f32_e32 v174, v174, v175
	v_add_f32_e32 v160, v160, v162
	v_add_f32_e32 v164, v164, v166
	v_add_f32_e32 v168, v168, v170
	v_add_f32_e32 v172, v172, v174
	v_add_f32_e32 v160, v160, v164
	v_add_f32_e32 v168, v168, v172
	v_add_f32_e32 v160, v160, v168
	v_add_f32_e32 v176, v176, v177
	v_add_f32_e32 v178, v178, v179
	v_add_f32_e32 v180, v180, v181
	v_add_f32_e32 v182, v182, v183
	v_add_f32_e32 v184, v184, v185
	v_add_f32_e32 v186, v186, v187
	v_add_f32_e32 v188, v188, v189
	v_add_f32_e32 v190, v190, v191
	v_add_f32_e32 v176, v176, v178
	v_add_f32_e32 v180, v180, v182
	v_add_f32_e32 v184, v184, v186
	v_add_f32_e32 v188, v188, v190
	v_add_f32_e32 v176, v176, v180
	v_add_f32_e32 v184, v184, v188
	v_add_f32_e32 v176, v176, v184
	v_fmamk_f32 v20, v128, 0x3aaaaaab, v31
	v_fmamk_f32 v22, v144, 0x3aaaaaab, v31
	v_fmamk_f32 v24, v160, 0x3aaaaaab, v31
	v_fmamk_f32 v26, v176, 0x3aaaaaab, v31
	v_rsq_f32_e32 v20, v20
	v_rsq_f32_e32 v22, v22
	v_rsq_f32_e32 v24, v24
	v_rsq_f32_e32 v26, v26
	s_nop 0
	v_mov_b32_e32 v128, 0
	v_mov_b32_e32 v129, 0
	v_mov_b32_e32 v130, 0
	v_mov_b32_e32 v131, 0
	v_mov_b32_e32 v132, 0
	v_mov_b32_e32 v133, 0
	v_mov_b32_e32 v134, 0
	v_mov_b32_e32 v135, 0
	v_mov_b32_e32 v136, 0
	v_mov_b32_e32 v137, 0
	v_mov_b32_e32 v138, 0
	v_mov_b32_e32 v139, 0
	v_mov_b32_e32 v140, 0
	v_mov_b32_e32 v141, 0
	v_mov_b32_e32 v142, 0
	v_mov_b32_e32 v143, 0
	v_mov_b32_e32 v144, 0
	v_mov_b32_e32 v145, 0
	v_mov_b32_e32 v146, 0
	v_mov_b32_e32 v147, 0
	v_mov_b32_e32 v148, 0
	v_mov_b32_e32 v149, 0
	v_mov_b32_e32 v150, 0
	v_mov_b32_e32 v151, 0
	v_mov_b32_e32 v152, 0
	v_mov_b32_e32 v153, 0
	v_mov_b32_e32 v154, 0
	v_mov_b32_e32 v155, 0
	v_mov_b32_e32 v156, 0
	v_mov_b32_e32 v157, 0
	v_mov_b32_e32 v158, 0
	v_mov_b32_e32 v159, 0
	v_mov_b32_e32 v160, 0
	v_mov_b32_e32 v161, 0
	v_mov_b32_e32 v162, 0
	v_mov_b32_e32 v163, 0
	v_mov_b32_e32 v164, 0
	v_mov_b32_e32 v165, 0
	v_mov_b32_e32 v166, 0
	v_mov_b32_e32 v167, 0
	v_mov_b32_e32 v168, 0
	v_mov_b32_e32 v169, 0
	v_mov_b32_e32 v170, 0
	v_mov_b32_e32 v171, 0
	v_mov_b32_e32 v172, 0
	v_mov_b32_e32 v173, 0
	v_mov_b32_e32 v174, 0
	v_mov_b32_e32 v175, 0
	v_mov_b32_e32 v176, 0
	v_mov_b32_e32 v177, 0
	v_mov_b32_e32 v178, 0
	v_mov_b32_e32 v179, 0
	v_mov_b32_e32 v180, 0
	v_mov_b32_e32 v181, 0
	v_mov_b32_e32 v182, 0
	v_mov_b32_e32 v183, 0
	v_mov_b32_e32 v184, 0
	v_mov_b32_e32 v185, 0
	v_mov_b32_e32 v186, 0
	v_mov_b32_e32 v187, 0
	v_mov_b32_e32 v188, 0
	v_mov_b32_e32 v189, 0
	v_mov_b32_e32 v190, 0
	v_mov_b32_e32 v191, 0
	v_mov_b32_e32 v192, 0
	v_mov_b32_e32 v193, 0
	v_mov_b32_e32 v194, 0
	v_mov_b32_e32 v195, 0
	v_mov_b32_e32 v196, 0
	v_mov_b32_e32 v197, 0
	v_mov_b32_e32 v198, 0
	v_mov_b32_e32 v199, 0
	v_mov_b32_e32 v200, 0
	v_mov_b32_e32 v201, 0
	v_mov_b32_e32 v202, 0
	v_mov_b32_e32 v203, 0
	v_mov_b32_e32 v204, 0
	v_mov_b32_e32 v205, 0
	v_mov_b32_e32 v206, 0
	v_mov_b32_e32 v207, 0
	v_mov_b32_e32 v208, 0
	v_mov_b32_e32 v209, 0
	v_mov_b32_e32 v210, 0
	v_mov_b32_e32 v211, 0
	v_mov_b32_e32 v212, 0
	v_mov_b32_e32 v213, 0
	v_mov_b32_e32 v214, 0
	v_mov_b32_e32 v215, 0
	v_mov_b32_e32 v216, 0
	v_mov_b32_e32 v217, 0
	v_mov_b32_e32 v218, 0
	v_mov_b32_e32 v219, 0
	v_mov_b32_e32 v220, 0
	v_mov_b32_e32 v221, 0
	v_mov_b32_e32 v222, 0
	v_mov_b32_e32 v223, 0
	v_mov_b32_e32 v224, 0
	v_mov_b32_e32 v225, 0
	v_mov_b32_e32 v226, 0
	v_mov_b32_e32 v227, 0
	v_mov_b32_e32 v228, 0
	v_mov_b32_e32 v229, 0
	v_mov_b32_e32 v230, 0
	v_mov_b32_e32 v231, 0
	v_mov_b32_e32 v232, 0
	v_mov_b32_e32 v233, 0
	v_mov_b32_e32 v234, 0
	v_mov_b32_e32 v235, 0
	v_mov_b32_e32 v236, 0
	v_mov_b32_e32 v237, 0
	v_mov_b32_e32 v238, 0
	v_mov_b32_e32 v239, 0
	v_mov_b32_e32 v240, 0
	v_mov_b32_e32 v241, 0
	v_mov_b32_e32 v242, 0
	v_mov_b32_e32 v243, 0
	v_mov_b32_e32 v244, 0
	v_mov_b32_e32 v245, 0
	v_mov_b32_e32 v246, 0
	v_mov_b32_e32 v247, 0
	v_mov_b32_e32 v248, 0
	v_mov_b32_e32 v249, 0
	v_mov_b32_e32 v250, 0
	v_mov_b32_e32 v251, 0
	v_mov_b32_e32 v252, 0
	v_mov_b32_e32 v253, 0
	v_mov_b32_e32 v254, 0
	v_mov_b32_e32 v255, 0
	s_waitcnt vmcnt(18)
	s_barrier
	v_add_u32_e32 v12, s21, v10
	v_add_u32_e32 v14, s21, v11
	v_xor_b32_e32 v13, 64, v12
	v_xor_b32_e32 v15, 64, v14
	s_add_u32 s21, s21, 0xc000
	s_sub_u32 s23, s21, 0x24000
	s_cmp_ge_u32 s21, 0x24000
	s_cselect_b32 s21, s23, s21
	ds_read_b128 v[32:35], v12 offset:0
	ds_read_b128 v[36:39], v12 offset:2048
	ds_read_b128 v[40:43], v12 offset:4096
	ds_read_b128 v[44:47], v12 offset:6144
	ds_read_b128 v[48:51], v14 offset:0
	ds_read_b128 v[52:55], v14 offset:2048
	ds_read_b128 v[56:59], v14 offset:4096
	ds_read_b128 v[60:63], v14 offset:6144
	ds_read_b128 v[64:67], v14 offset:8192
	ds_read_b128 v[68:71], v14 offset:10240
	ds_read_b128 v[72:75], v14 offset:12288
	ds_read_b128 v[76:79], v14 offset:14336
	s_mov_b32 s15, 0
.Lup_loop:
	s_waitcnt lgkmcnt(0)
	v_mfma_f32_16x16x32_bf16 v[128:131], v[48:51], v[32:35], v[128:131]
	ds_read_b128 v[80:83], v13 offset:0
	v_mfma_f32_16x16x32_bf16 v[132:135], v[48:51], v[36:39], v[132:135]
	s_add_u32 m0, s20, 0x6000
	v_mfma_f32_16x16x32_bf16 v[136:139], v[48:51], v[40:43], v[136:139]
	ds_read_b128 v[84:87], v13 offset:2048
	v_mfma_f32_16x16x32_bf16 v[140:143], v[48:51], v[44:47], v[140:143]
	global_load_lds_dwordx4 v4, s[18:19]
	v_mfma_f32_16x16x32_bf16 v[144:147], v[52:55], v[32:35], v[144:147]
	ds_read_b128 v[88:91], v13 offset:4096
	v_mfma_f32_16x16x32_bf16 v[148:151], v[52:55], v[36:39], v[148:151]
	s_add_u32 m0, s20, 0x7000
	v_mfma_f32_16x16x32_bf16 v[152:155], v[52:55], v[40:43], v[152:155]
	ds_read_b128 v[92:95], v13 offset:6144
	v_mfma_f32_16x16x32_bf16 v[156:159], v[52:55], v[44:47], v[156:159]
	global_load_lds_dwordx4 v5, s[18:19]
	v_mfma_f32_16x16x32_bf16 v[160:163], v[56:59], v[32:35], v[160:163]
	ds_read_b128 v[96:99], v15 offset:0
	v_mfma_f32_16x16x32_bf16 v[164:167], v[56:59], v[36:39], v[164:167]
	s_add_u32 m0, s20, 0x8000
	v_mfma_f32_16x16x32_bf16 v[168:171], v[56:59], v[40:43], v[168:171]
	ds_read_b128 v[100:103], v15 offset:2048
	v_mfma_f32_16x16x32_bf16 v[172:175], v[56:59], v[44:47], v[172:175]
	global_load_lds_dwordx4 v6, s[18:19]
	v_mfma_f32_16x16x32_bf16 v[176:179], v[60:63], v[32:35], v[176:179]
	ds_read_b128 v[104:107], v15 offset:4096
	v_mfma_f32_16x16x32_bf16 v[180:183], v[60:63], v[36:39], v[180:183]
	s_add_u32 m0, s20, 0x9000
	v_mfma_f32_16x16x32_bf16 v[184:187], v[60:63], v[40:43], v[184:187]
	ds_read_b128 v[108:111], v15 offset:6144
	v_mfma_f32_16x16x32_bf16 v[188:191], v[60:63], v[44:47], v[188:191]
	global_load_lds_dwordx4 v7, s[18:19]
	v_mfma_f32_16x16x32_bf16 v[192:195], v[64:67], v[32:35], v[192:195]
	ds_read_b128 v[112:115], v15 offset:8192
	v_mfma_f32_16x16x32_bf16 v[196:199], v[64:67], v[36:39], v[196:199]
	s_add_u32 m0, s20, 0xa000
	v_mfma_f32_16x16x32_bf16 v[200:203], v[64:67], v[40:43], v[200:203]
	ds_read_b128 v[116:119], v15 offset:10240
	v_mfma_f32_16x16x32_bf16 v[204:207], v[64:67], v[44:47], v[204:207]
	global_load_lds_dwordx4 v8, s[18:19]
	v_mfma_f32_16x16x32_bf16 v[208:211], v[68:71], v[32:35], v[208:211]
	ds_read_b128 v[120:123], v15 offset:12288
	v_mfma_f32_16x16x32_bf16 v[212:215], v[68:71], v[36:39], v[212:215]
	s_add_u32 m0, s20, 0xb000
	v_mfma_f32_16x16x32_bf16 v[216:219], v[68:71], v[40:43], v[216:219]
	ds_read_b128 v[124:127], v15 offset:14336
	v_mfma_f32_16x16x32_bf16 v[220:223], v[68:71], v[44:47], v[220:223]
	global_load_lds_dwordx4 v9, s[18:19]
	v_mfma_f32_16x16x32_bf16 v[224:227], v[72:75], v[32:35], v[224:227]
	v_mfma_f32_16x16x32_bf16 v[228:231], v[72:75], v[36:39], v[228:231]
	v_mfma_f32_16x16x32_bf16 v[232:235], v[72:75], v[40:43], v[232:235]
	v_mfma_f32_16x16x32_bf16 v[236:239], v[72:75], v[44:47], v[236:239]
	v_mfma_f32_16x16x32_bf16 v[240:243], v[76:79], v[32:35], v[240:243]
	s_add_u32 s16, s16, 0x80
	s_addc_u32 s17, s17, 0
	s_add_u32 s18, s18, 0x80
	s_addc_u32 s19, s19, 0
	v_mfma_f32_16x16x32_bf16 v[244:247], v[76:79], v[36:39], v[244:247]
	s_add_u32 s20, s20, 0xc000
	s_sub_u32 s22, s20, 0x24000
	s_cmp_ge_u32 s20, 0x24000
	s_cselect_b32 s20, s22, s20
	v_mfma_f32_16x16x32_bf16 v[248:251], v[76:79], v[40:43], v[248:251]
	v_add_u32_e32 v12, s21, v10
	v_add_u32_e32 v14, s21, v11
	v_xor_b32_e32 v13, 64, v12
	v_xor_b32_e32 v15, 64, v14
	v_mfma_f32_16x16x32_bf16 v[252:255], v[76:79], v[44:47], v[252:255]
	s_add_u32 s21, s21, 0xc000
	s_sub_u32 s23, s21, 0x24000
	s_cmp_ge_u32 s21, 0x24000
	s_cselect_b32 s21, s23, s21
	s_waitcnt vmcnt(12) lgkmcnt(0)
	s_barrier
	v_mfma_f32_16x16x32_bf16 v[128:131], v[96:99], v[80:83], v[128:131]
	ds_read_b128 v[32:35], v12 offset:0
	v_mfma_f32_16x16x32_bf16 v[132:135], v[96:99], v[84:87], v[132:135]
	s_add_u32 m0, s20, 0x0
	v_mfma_f32_16x16x32_bf16 v[136:139], v[96:99], v[88:91], v[136:139]
	ds_read_b128 v[36:39], v12 offset:2048
	v_mfma_f32_16x16x32_bf16 v[140:143], v[96:99], v[92:95], v[140:143]
	global_load_lds_dwordx4 v2, s[16:17]
	v_mfma_f32_16x16x32_bf16 v[144:147], v[100:103], v[80:83], v[144:147]
	ds_read_b128 v[40:43], v12 offset:4096
	v_mfma_f32_16x16x32_bf16 v[148:151], v[100:103], v[84:87], v[148:151]
	s_add_u32 m0, s20, 0x1000
	v_mfma_f32_16x16x32_bf16 v[152:155], v[100:103], v[88:91], v[152:155]
	ds_read_b128 v[44:47], v12 offset:6144
	v_mfma_f32_16x16x32_bf16 v[156:159], v[100:103], v[92:95], v[156:159]
	global_load_lds_dwordx4 v3, s[16:17]
	v_mfma_f32_16x16x32_bf16 v[160:163], v[104:107], v[80:83], v[160:163]
	ds_read_b128 v[48:51], v14 offset:0
	v_mfma_f32_16x16x32_bf16 v[164:167], v[104:107], v[84:87], v[164:167]
	s_add_u32 m0, s20, 0x2000
	v_mfma_f32_16x16x32_bf16 v[168:171], v[104:107], v[88:91], v[168:171]
	ds_read_b128 v[52:55], v14 offset:2048
	v_mfma_f32_16x16x32_bf16 v[172:175], v[104:107], v[92:95], v[172:175]
	global_load_lds_dwordx4 v4, s[16:17]
	v_mfma_f32_16x16x32_bf16 v[176:179], v[108:111], v[80:83], v[176:179]
	ds_read_b128 v[56:59], v14 offset:4096
	v_mfma_f32_16x16x32_bf16 v[180:183], v[108:111], v[84:87], v[180:183]
	s_add_u32 m0, s20, 0x3000
	v_mfma_f32_16x16x32_bf16 v[184:187], v[108:111], v[88:91], v[184:187]
	ds_read_b128 v[60:63], v14 offset:6144
	v_mfma_f32_16x16x32_bf16 v[188:191], v[108:111], v[92:95], v[188:191]
	global_load_lds_dwordx4 v5, s[16:17]
	v_mfma_f32_16x16x32_bf16 v[192:195], v[112:115], v[80:83], v[192:195]
	ds_read_b128 v[64:67], v14 offset:8192
	v_mfma_f32_16x16x32_bf16 v[196:199], v[112:115], v[84:87], v[196:199]
	s_add_u32 m0, s20, 0x4000
	v_mfma_f32_16x16x32_bf16 v[200:203], v[112:115], v[88:91], v[200:203]
	ds_read_b128 v[68:71], v14 offset:10240
	v_mfma_f32_16x16x32_bf16 v[204:207], v[112:115], v[92:95], v[204:207]
	global_load_lds_dwordx4 v2, s[18:19]
	v_mfma_f32_16x16x32_bf16 v[208:211], v[116:119], v[80:83], v[208:211]
	ds_read_b128 v[72:75], v14 offset:12288
	v_mfma_f32_16x16x32_bf16 v[212:215], v[116:119], v[84:87], v[212:215]
	s_add_u32 m0, s20, 0x5000
	v_mfma_f32_16x16x32_bf16 v[216:219], v[116:119], v[88:91], v[216:219]
	ds_read_b128 v[76:79], v14 offset:14336
	v_mfma_f32_16x16x32_bf16 v[220:223], v[116:119], v[92:95], v[220:223]
	global_load_lds_dwordx4 v3, s[18:19]
	v_mfma_f32_16x16x32_bf16 v[224:227], v[120:123], v[80:83], v[224:227]
	v_mfma_f32_16x16x32_bf16 v[228:231], v[120:123], v[84:87], v[228:231]
	v_mfma_f32_16x16x32_bf16 v[232:235], v[120:123], v[88:91], v[232:235]
	v_mfma_f32_16x16x32_bf16 v[236:239], v[120:123], v[92:95], v[236:239]
	v_mfma_f32_16x16x32_bf16 v[240:243], v[124:127], v[80:83], v[240:243]
	v_mfma_f32_16x16x32_bf16 v[244:247], v[124:127], v[84:87], v[244:247]
	v_mfma_f32_16x16x32_bf16 v[248:251], v[124:127], v[88:91], v[248:251]
	v_mfma_f32_16x16x32_bf16 v[252:255], v[124:127], v[92:95], v[252:255]
	s_add_u32 s15, s15, 1
	s_cmp_lt_u32 s15, 9
	s_cbranch_scc1 .Lup_loop
	s_waitcnt lgkmcnt(0)
	v_mfma_f32_16x16x32_bf16 v[128:131], v[48:51], v[32:35], v[128:131]
	ds_read_b128 v[80:83], v13 offset:0
	v_mfma_f32_16x16x32_bf16 v[132:135], v[48:51], v[36:39], v[132:135]
	s_add_u32 m0, s20, 0x6000
	v_mfma_f32_16x16x32_bf16 v[136:139], v[48:51], v[40:43], v[136:139]
	ds_read_b128 v[84:87], v13 offset:2048
	v_mfma_f32_16x16x32_bf16 v[140:143], v[48:51], v[44:47], v[140:143]
	global_load_lds_dwordx4 v4, s[18:19]
	v_mfma_f32_16x16x32_bf16 v[144:147], v[52:55], v[32:35], v[144:147]
	ds_read_b128 v[88:91], v13 offset:4096
	v_mfma_f32_16x16x32_bf16 v[148:151], v[52:55], v[36:39], v[148:151]
	s_add_u32 m0, s20, 0x7000
	v_mfma_f32_16x16x32_bf16 v[152:155], v[52:55], v[40:43], v[152:155]
	ds_read_b128 v[92:95], v13 offset:6144
	v_mfma_f32_16x16x32_bf16 v[156:159], v[52:55], v[44:47], v[156:159]
	global_load_lds_dwordx4 v5, s[18:19]
	v_mfma_f32_16x16x32_bf16 v[160:163], v[56:59], v[32:35], v[160:163]
	ds_read_b128 v[96:99], v15 offset:0
	v_mfma_f32_16x16x32_bf16 v[164:167], v[56:59], v[36:39], v[164:167]
	s_add_u32 m0, s20, 0x8000
	v_mfma_f32_16x16x32_bf16 v[168:171], v[56:59], v[40:43], v[168:171]
	ds_read_b128 v[100:103], v15 offset:2048
	v_mfma_f32_16x16x32_bf16 v[172:175], v[56:59], v[44:47], v[172:175]
	global_load_lds_dwordx4 v6, s[18:19]
	v_mfma_f32_16x16x32_bf16 v[176:179], v[60:63], v[32:35], v[176:179]
	ds_read_b128 v[104:107], v15 offset:4096
	v_mfma_f32_16x16x32_bf16 v[180:183], v[60:63], v[36:39], v[180:183]
	s_add_u32 m0, s20, 0x9000
	v_mfma_f32_16x16x32_bf16 v[184:187], v[60:63], v[40:43], v[184:187]
	ds_read_b128 v[108:111], v15 offset:6144
	v_mfma_f32_16x16x32_bf16 v[188:191], v[60:63], v[44:47], v[188:191]
	global_load_lds_dwordx4 v7, s[18:19]
	v_mfma_f32_16x16x32_bf16 v[192:195], v[64:67], v[32:35], v[192:195]
	ds_read_b128 v[112:115], v15 offset:8192
	v_mfma_f32_16x16x32_bf16 v[196:199], v[64:67], v[36:39], v[196:199]
	s_add_u32 m0, s20, 0xa000
	v_mfma_f32_16x16x32_bf16 v[200:203], v[64:67], v[40:43], v[200:203]
	ds_read_b128 v[116:119], v15 offset:10240
	v_mfma_f32_16x16x32_bf16 v[204:207], v[64:67], v[44:47], v[204:207]
	global_load_lds_dwordx4 v8, s[18:19]
	v_mfma_f32_16x16x32_bf16 v[208:211], v[68:71], v[32:35], v[208:211]
	ds_read_b128 v[120:123], v15 offset:12288
	v_mfma_f32_16x16x32_bf16 v[212:215], v[68:71], v[36:39], v[212:215]
	s_add_u32 m0, s20, 0xb000
	v_mfma_f32_16x16x32_bf16 v[216:219], v[68:71], v[40:43], v[216:219]
	ds_read_b128 v[124:127], v15 offset:14336
	v_mfma_f32_16x16x32_bf16 v[220:223], v[68:71], v[44:47], v[220:223]
	global_load_lds_dwordx4 v9, s[18:19]
	v_mfma_f32_16x16x32_bf16 v[224:227], v[72:75], v[32:35], v[224:227]
	v_mfma_f32_16x16x32_bf16 v[228:231], v[72:75], v[36:39], v[228:231]
	v_mfma_f32_16x16x32_bf16 v[232:235], v[72:75], v[40:43], v[232:235]
	v_mfma_f32_16x16x32_bf16 v[236:239], v[72:75], v[44:47], v[236:239]
	v_mfma_f32_16x16x32_bf16 v[240:243], v[76:79], v[32:35], v[240:243]
	s_add_u32 s16, s16, 0x80
	s_addc_u32 s17, s17, 0
	s_add_u32 s18, s18, 0x80
	s_addc_u32 s19, s19, 0
	v_mfma_f32_16x16x32_bf16 v[244:247], v[76:79], v[36:39], v[244:247]
	s_add_u32 s20, s20, 0xc000
	s_sub_u32 s22, s20, 0x24000
	s_cmp_ge_u32 s20, 0x24000
	s_cselect_b32 s20, s22, s20
	v_mfma_f32_16x16x32_bf16 v[248:251], v[76:79], v[40:43], v[248:251]
	v_add_u32_e32 v12, s21, v10
	v_add_u32_e32 v14, s21, v11
	v_xor_b32_e32 v13, 64, v12
	v_xor_b32_e32 v15, 64, v14
	v_mfma_f32_16x16x32_bf16 v[252:255], v[76:79], v[44:47], v[252:255]
	s_add_u32 s21, s21, 0xc000
	s_sub_u32 s23, s21, 0x24000
	s_cmp_ge_u32 s21, 0x24000
	s_cselect_b32 s21, s23, s21
	s_waitcnt vmcnt(12) lgkmcnt(0)
	s_barrier
	v_mfma_f32_16x16x32_bf16 v[128:131], v[96:99], v[80:83], v[128:131]
	ds_read_b128 v[32:35], v12 offset:0
	v_mfma_f32_16x16x32_bf16 v[132:135], v[96:99], v[84:87], v[132:135]
	ds_read_b128 v[36:39], v12 offset:2048
	v_mfma_f32_16x16x32_bf16 v[136:139], v[96:99], v[88:91], v[136:139]
	ds_read_b128 v[40:43], v12 offset:4096
	v_mfma_f32_16x16x32_bf16 v[140:143], v[96:99], v[92:95], v[140:143]
	ds_read_b128 v[44:47], v12 offset:6144
	v_mfma_f32_16x16x32_bf16 v[144:147], v[100:103], v[80:83], v[144:147]
	ds_read_b128 v[48:51], v14 offset:0
	v_mfma_f32_16x16x32_bf16 v[148:151], v[100:103], v[84:87], v[148:151]
	ds_read_b128 v[52:55], v14 offset:2048
	v_mfma_f32_16x16x32_bf16 v[152:155], v[100:103], v[88:91], v[152:155]
	ds_read_b128 v[56:59], v14 offset:4096
	v_mfma_f32_16x16x32_bf16 v[156:159], v[100:103], v[92:95], v[156:159]
	ds_read_b128 v[60:63], v14 offset:6144
	v_mfma_f32_16x16x32_bf16 v[160:163], v[104:107], v[80:83], v[160:163]
	ds_read_b128 v[64:67], v14 offset:8192
	v_mfma_f32_16x16x32_bf16 v[164:167], v[104:107], v[84:87], v[164:167]
	ds_read_b128 v[68:71], v14 offset:10240
	v_mfma_f32_16x16x32_bf16 v[168:171], v[104:107], v[88:91], v[168:171]
	ds_read_b128 v[72:75], v14 offset:12288
	v_mfma_f32_16x16x32_bf16 v[172:175], v[104:107], v[92:95], v[172:175]
	ds_read_b128 v[76:79], v14 offset:14336
	v_mfma_f32_16x16x32_bf16 v[176:179], v[108:111], v[80:83], v[176:179]
	v_mfma_f32_16x16x32_bf16 v[180:183], v[108:111], v[84:87], v[180:183]
	v_mfma_f32_16x16x32_bf16 v[184:187], v[108:111], v[88:91], v[184:187]
	v_mfma_f32_16x16x32_bf16 v[188:191], v[108:111], v[92:95], v[188:191]
	v_mfma_f32_16x16x32_bf16 v[192:195], v[112:115], v[80:83], v[192:195]
	v_mfma_f32_16x16x32_bf16 v[196:199], v[112:115], v[84:87], v[196:199]
	v_mfma_f32_16x16x32_bf16 v[200:203], v[112:115], v[88:91], v[200:203]
	v_mfma_f32_16x16x32_bf16 v[204:207], v[112:115], v[92:95], v[204:207]
	v_mfma_f32_16x16x32_bf16 v[208:211], v[116:119], v[80:83], v[208:211]
	v_mfma_f32_16x16x32_bf16 v[212:215], v[116:119], v[84:87], v[212:215]
	v_mfma_f32_16x16x32_bf16 v[216:219], v[116:119], v[88:91], v[216:219]
	v_mfma_f32_16x16x32_bf16 v[220:223], v[116:119], v[92:95], v[220:223]
	v_mfma_f32_16x16x32_bf16 v[224:227], v[120:123], v[80:83], v[224:227]
	v_mfma_f32_16x16x32_bf16 v[228:231], v[120:123], v[84:87], v[228:231]
	v_mfma_f32_16x16x32_bf16 v[232:235], v[120:123], v[88:91], v[232:235]
	v_mfma_f32_16x16x32_bf16 v[236:239], v[120:123], v[92:95], v[236:239]
	v_mfma_f32_16x16x32_bf16 v[240:243], v[124:127], v[80:83], v[240:243]
	v_mfma_f32_16x16x32_bf16 v[244:247], v[124:127], v[84:87], v[244:247]
	v_mfma_f32_16x16x32_bf16 v[248:251], v[124:127], v[88:91], v[248:251]
	v_mfma_f32_16x16x32_bf16 v[252:255], v[124:127], v[92:95], v[252:255]
	s_waitcnt lgkmcnt(0)
	v_mfma_f32_16x16x32_bf16 v[128:131], v[48:51], v[32:35], v[128:131]
	ds_read_b128 v[80:83], v13 offset:0
	v_mfma_f32_16x16x32_bf16 v[132:135], v[48:51], v[36:39], v[132:135]
	ds_read_b128 v[84:87], v13 offset:2048
	v_mfma_f32_16x16x32_bf16 v[136:139], v[48:51], v[40:43], v[136:139]
	ds_read_b128 v[88:91], v13 offset:4096
	v_mfma_f32_16x16x32_bf16 v[140:143], v[48:51], v[44:47], v[140:143]
	ds_read_b128 v[92:95], v13 offset:6144
	v_mfma_f32_16x16x32_bf16 v[144:147], v[52:55], v[32:35], v[144:147]
	ds_read_b128 v[96:99], v15 offset:0
	v_mfma_f32_16x16x32_bf16 v[148:151], v[52:55], v[36:39], v[148:151]
	ds_read_b128 v[100:103], v15 offset:2048
	v_mfma_f32_16x16x32_bf16 v[152:155], v[52:55], v[40:43], v[152:155]
	ds_read_b128 v[104:107], v15 offset:4096
	v_mfma_f32_16x16x32_bf16 v[156:159], v[52:55], v[44:47], v[156:159]
	ds_read_b128 v[108:111], v15 offset:6144
	v_mfma_f32_16x16x32_bf16 v[160:163], v[56:59], v[32:35], v[160:163]
	ds_read_b128 v[112:115], v15 offset:8192
	v_mfma_f32_16x16x32_bf16 v[164:167], v[56:59], v[36:39], v[164:167]
	ds_read_b128 v[116:119], v15 offset:10240
	v_mfma_f32_16x16x32_bf16 v[168:171], v[56:59], v[40:43], v[168:171]
	ds_read_b128 v[120:123], v15 offset:12288
	v_mfma_f32_16x16x32_bf16 v[172:175], v[56:59], v[44:47], v[172:175]
	ds_read_b128 v[124:127], v15 offset:14336
	v_mfma_f32_16x16x32_bf16 v[176:179], v[60:63], v[32:35], v[176:179]
	v_mfma_f32_16x16x32_bf16 v[180:183], v[60:63], v[36:39], v[180:183]
	v_mfma_f32_16x16x32_bf16 v[184:187], v[60:63], v[40:43], v[184:187]
	v_mfma_f32_16x16x32_bf16 v[188:191], v[60:63], v[44:47], v[188:191]
	v_mfma_f32_16x16x32_bf16 v[192:195], v[64:67], v[32:35], v[192:195]
	v_mfma_f32_16x16x32_bf16 v[196:199], v[64:67], v[36:39], v[196:199]
	v_mfma_f32_16x16x32_bf16 v[200:203], v[64:67], v[40:43], v[200:203]
	v_mfma_f32_16x16x32_bf16 v[204:207], v[64:67], v[44:47], v[204:207]
	v_mfma_f32_16x16x32_bf16 v[208:211], v[68:71], v[32:35], v[208:211]
	v_mfma_f32_16x16x32_bf16 v[212:215], v[68:71], v[36:39], v[212:215]
	v_mfma_f32_16x16x32_bf16 v[216:219], v[68:71], v[40:43], v[216:219]
	v_mfma_f32_16x16x32_bf16 v[220:223], v[68:71], v[44:47], v[220:223]
	v_mfma_f32_16x16x32_bf16 v[224:227], v[72:75], v[32:35], v[224:227]
	v_mfma_f32_16x16x32_bf16 v[228:231], v[72:75], v[36:39], v[228:231]
	v_mfma_f32_16x16x32_bf16 v[232:235], v[72:75], v[40:43], v[232:235]
	v_mfma_f32_16x16x32_bf16 v[236:239], v[72:75], v[44:47], v[236:239]
	v_mfma_f32_16x16x32_bf16 v[240:243], v[76:79], v[32:35], v[240:243]
	v_add_u32_e32 v12, s21, v10
	v_add_u32_e32 v14, s21, v11
	v_xor_b32_e32 v13, 64, v12
	v_xor_b32_e32 v15, 64, v14
	v_mfma_f32_16x16x32_bf16 v[244:247], v[76:79], v[36:39], v[244:247]
	s_add_u32 s21, s21, 0xc000
	s_sub_u32 s23, s21, 0x24000
	s_cmp_ge_u32 s21, 0x24000
	s_cselect_b32 s21, s23, s21
	v_mfma_f32_16x16x32_bf16 v[248:251], v[76:79], v[40:43], v[248:251]
	v_mfma_f32_16x16x32_bf16 v[252:255], v[76:79], v[44:47], v[252:255]
	s_waitcnt vmcnt(0) lgkmcnt(0)
	s_barrier
	v_mfma_f32_16x16x32_bf16 v[128:131], v[96:99], v[80:83], v[128:131]
	ds_read_b128 v[32:35], v12 offset:0
	v_mfma_f32_16x16x32_bf16 v[132:135], v[96:99], v[84:87], v[132:135]
	ds_read_b128 v[36:39], v12 offset:2048
	v_mfma_f32_16x16x32_bf16 v[136:139], v[96:99], v[88:91], v[136:139]
	ds_read_b128 v[40:43], v12 offset:4096
	v_mfma_f32_16x16x32_bf16 v[140:143], v[96:99], v[92:95], v[140:143]
	ds_read_b128 v[44:47], v12 offset:6144
	v_mfma_f32_16x16x32_bf16 v[144:147], v[100:103], v[80:83], v[144:147]
	ds_read_b128 v[48:51], v14 offset:0
	v_mfma_f32_16x16x32_bf16 v[148:151], v[100:103], v[84:87], v[148:151]
	ds_read_b128 v[52:55], v14 offset:2048
	v_mfma_f32_16x16x32_bf16 v[152:155], v[100:103], v[88:91], v[152:155]
	ds_read_b128 v[56:59], v14 offset:4096
	v_mfma_f32_16x16x32_bf16 v[156:159], v[100:103], v[92:95], v[156:159]
	ds_read_b128 v[60:63], v14 offset:6144
	v_mfma_f32_16x16x32_bf16 v[160:163], v[104:107], v[80:83], v[160:163]
	ds_read_b128 v[64:67], v14 offset:8192
	v_mfma_f32_16x16x32_bf16 v[164:167], v[104:107], v[84:87], v[164:167]
	ds_read_b128 v[68:71], v14 offset:10240
	v_mfma_f32_16x16x32_bf16 v[168:171], v[104:107], v[88:91], v[168:171]
	ds_read_b128 v[72:75], v14 offset:12288
	v_mfma_f32_16x16x32_bf16 v[172:175], v[104:107], v[92:95], v[172:175]
	ds_read_b128 v[76:79], v14 offset:14336
	v_mfma_f32_16x16x32_bf16 v[176:179], v[108:111], v[80:83], v[176:179]
	v_mfma_f32_16x16x32_bf16 v[180:183], v[108:111], v[84:87], v[180:183]
	v_mfma_f32_16x16x32_bf16 v[184:187], v[108:111], v[88:91], v[184:187]
	v_mfma_f32_16x16x32_bf16 v[188:191], v[108:111], v[92:95], v[188:191]
	v_mfma_f32_16x16x32_bf16 v[192:195], v[112:115], v[80:83], v[192:195]
	v_mfma_f32_16x16x32_bf16 v[196:199], v[112:115], v[84:87], v[196:199]
	v_mfma_f32_16x16x32_bf16 v[200:203], v[112:115], v[88:91], v[200:203]
	v_mfma_f32_16x16x32_bf16 v[204:207], v[112:115], v[92:95], v[204:207]
	v_mfma_f32_16x16x32_bf16 v[208:211], v[116:119], v[80:83], v[208:211]
	v_mfma_f32_16x16x32_bf16 v[212:215], v[116:119], v[84:87], v[212:215]
	v_mfma_f32_16x16x32_bf16 v[216:219], v[116:119], v[88:91], v[216:219]
	v_mfma_f32_16x16x32_bf16 v[220:223], v[116:119], v[92:95], v[220:223]
	v_mfma_f32_16x16x32_bf16 v[224:227], v[120:123], v[80:83], v[224:227]
	v_mfma_f32_16x16x32_bf16 v[228:231], v[120:123], v[84:87], v[228:231]
	v_mfma_f32_16x16x32_bf16 v[232:235], v[120:123], v[88:91], v[232:235]
	v_mfma_f32_16x16x32_bf16 v[236:239], v[120:123], v[92:95], v[236:239]
	v_mfma_f32_16x16x32_bf16 v[240:243], v[124:127], v[80:83], v[240:243]
	v_mfma_f32_16x16x32_bf16 v[244:247], v[124:127], v[84:87], v[244:247]
	v_mfma_f32_16x16x32_bf16 v[248:251], v[124:127], v[88:91], v[248:251]
	v_mfma_f32_16x16x32_bf16 v[252:255], v[124:127], v[92:95], v[252:255]
	s_waitcnt lgkmcnt(0)
	v_mfma_f32_16x16x32_bf16 v[128:131], v[48:51], v[32:35], v[128:131]
	ds_read_b128 v[80:83], v13 offset:0
	v_mfma_f32_16x16x32_bf16 v[132:135], v[48:51], v[36:39], v[132:135]
	ds_read_b128 v[84:87], v13 offset:2048
	v_mfma_f32_16x16x32_bf16 v[136:139], v[48:51], v[40:43], v[136:139]
	ds_read_b128 v[88:91], v13 offset:4096
	v_mfma_f32_16x16x32_bf16 v[140:143], v[48:51], v[44:47], v[140:143]
	ds_read_b128 v[92:95], v13 offset:6144
	v_mfma_f32_16x16x32_bf16 v[144:147], v[52:55], v[32:35], v[144:147]
	ds_read_b128 v[96:99], v15 offset:0
	v_mfma_f32_16x16x32_bf16 v[148:151], v[52:55], v[36:39], v[148:151]
	ds_read_b128 v[100:103], v15 offset:2048
	v_mfma_f32_16x16x32_bf16 v[152:155], v[52:55], v[40:43], v[152:155]
	ds_read_b128 v[104:107], v15 offset:4096
	v_mfma_f32_16x16x32_bf16 v[156:159], v[52:55], v[44:47], v[156:159]
	ds_read_b128 v[108:111], v15 offset:6144
	v_mfma_f32_16x16x32_bf16 v[160:163], v[56:59], v[32:35], v[160:163]
	ds_read_b128 v[112:115], v15 offset:8192
	v_mfma_f32_16x16x32_bf16 v[164:167], v[56:59], v[36:39], v[164:167]
	ds_read_b128 v[116:119], v15 offset:10240
	v_mfma_f32_16x16x32_bf16 v[168:171], v[56:59], v[40:43], v[168:171]
	ds_read_b128 v[120:123], v15 offset:12288
	v_mfma_f32_16x16x32_bf16 v[172:175], v[56:59], v[44:47], v[172:175]
	ds_read_b128 v[124:127], v15 offset:14336
	v_mfma_f32_16x16x32_bf16 v[176:179], v[60:63], v[32:35], v[176:179]
	v_mfma_f32_16x16x32_bf16 v[180:183], v[60:63], v[36:39], v[180:183]
	v_mfma_f32_16x16x32_bf16 v[184:187], v[60:63], v[40:43], v[184:187]
	v_mfma_f32_16x16x32_bf16 v[188:191], v[60:63], v[44:47], v[188:191]
	v_mfma_f32_16x16x32_bf16 v[192:195], v[64:67], v[32:35], v[192:195]
	v_mfma_f32_16x16x32_bf16 v[196:199], v[64:67], v[36:39], v[196:199]
	v_mfma_f32_16x16x32_bf16 v[200:203], v[64:67], v[40:43], v[200:203]
	v_mfma_f32_16x16x32_bf16 v[204:207], v[64:67], v[44:47], v[204:207]
	v_mfma_f32_16x16x32_bf16 v[208:211], v[68:71], v[32:35], v[208:211]
	v_mfma_f32_16x16x32_bf16 v[212:215], v[68:71], v[36:39], v[212:215]
	v_mfma_f32_16x16x32_bf16 v[216:219], v[68:71], v[40:43], v[216:219]
	v_mfma_f32_16x16x32_bf16 v[220:223], v[68:71], v[44:47], v[220:223]
	v_mfma_f32_16x16x32_bf16 v[224:227], v[72:75], v[32:35], v[224:227]
	v_mfma_f32_16x16x32_bf16 v[228:231], v[72:75], v[36:39], v[228:231]
	v_mfma_f32_16x16x32_bf16 v[232:235], v[72:75], v[40:43], v[232:235]
	v_mfma_f32_16x16x32_bf16 v[236:239], v[72:75], v[44:47], v[236:239]
	v_mfma_f32_16x16x32_bf16 v[240:243], v[76:79], v[32:35], v[240:243]
	v_mfma_f32_16x16x32_bf16 v[244:247], v[76:79], v[36:39], v[244:247]
	v_mfma_f32_16x16x32_bf16 v[248:251], v[76:79], v[40:43], v[248:251]
	v_mfma_f32_16x16x32_bf16 v[252:255], v[76:79], v[44:47], v[252:255]
	s_waitcnt lgkmcnt(0)
	v_mfma_f32_16x16x32_bf16 v[128:131], v[96:99], v[80:83], v[128:131]
	v_mfma_f32_16x16x32_bf16 v[132:135], v[96:99], v[84:87], v[132:135]
	v_mfma_f32_16x16x32_bf16 v[136:139], v[96:99], v[88:91], v[136:139]
	v_mfma_f32_16x16x32_bf16 v[140:143], v[96:99], v[92:95], v[140:143]
	v_mfma_f32_16x16x32_bf16 v[144:147], v[100:103], v[80:83], v[144:147]
	v_mfma_f32_16x16x32_bf16 v[148:151], v[100:103], v[84:87], v[148:151]
	v_mfma_f32_16x16x32_bf16 v[152:155], v[100:103], v[88:91], v[152:155]
	v_mfma_f32_16x16x32_bf16 v[156:159], v[100:103], v[92:95], v[156:159]
	v_mfma_f32_16x16x32_bf16 v[160:163], v[104:107], v[80:83], v[160:163]
	v_mfma_f32_16x16x32_bf16 v[164:167], v[104:107], v[84:87], v[164:167]
	v_mfma_f32_16x16x32_bf16 v[168:171], v[104:107], v[88:91], v[168:171]
	v_mfma_f32_16x16x32_bf16 v[172:175], v[104:107], v[92:95], v[172:175]
	v_mfma_f32_16x16x32_bf16 v[176:179], v[108:111], v[80:83], v[176:179]
	v_mfma_f32_16x16x32_bf16 v[180:183], v[108:111], v[84:87], v[180:183]
	v_mfma_f32_16x16x32_bf16 v[184:187], v[108:111], v[88:91], v[184:187]
	v_mfma_f32_16x16x32_bf16 v[188:191], v[108:111], v[92:95], v[188:191]
	v_mfma_f32_16x16x32_bf16 v[192:195], v[112:115], v[80:83], v[192:195]
	v_mfma_f32_16x16x32_bf16 v[196:199], v[112:115], v[84:87], v[196:199]
	v_mfma_f32_16x16x32_bf16 v[200:203], v[112:115], v[88:91], v[200:203]
	v_mfma_f32_16x16x32_bf16 v[204:207], v[112:115], v[92:95], v[204:207]
	v_mfma_f32_16x16x32_bf16 v[208:211], v[116:119], v[80:83], v[208:211]
	v_mfma_f32_16x16x32_bf16 v[212:215], v[116:119], v[84:87], v[212:215]
	v_mfma_f32_16x16x32_bf16 v[216:219], v[116:119], v[88:91], v[216:219]
	v_mfma_f32_16x16x32_bf16 v[220:223], v[116:119], v[92:95], v[220:223]
	v_mfma_f32_16x16x32_bf16 v[224:227], v[120:123], v[80:83], v[224:227]
	v_mfma_f32_16x16x32_bf16 v[228:231], v[120:123], v[84:87], v[228:231]
	v_mfma_f32_16x16x32_bf16 v[232:235], v[120:123], v[88:91], v[232:235]
	v_mfma_f32_16x16x32_bf16 v[236:239], v[120:123], v[92:95], v[236:239]
	v_mfma_f32_16x16x32_bf16 v[240:243], v[124:127], v[80:83], v[240:243]
	v_mfma_f32_16x16x32_bf16 v[244:247], v[124:127], v[84:87], v[244:247]
	v_mfma_f32_16x16x32_bf16 v[248:251], v[124:127], v[88:91], v[248:251]
	v_mfma_f32_16x16x32_bf16 v[252:255], v[124:127], v[92:95], v[252:255]
	v_pk_mul_f32 v[128:129], v[128:129], v[20:21] op_sel_hi:[1,0]
	v_pk_mul_f32 v[130:131], v[130:131], v[20:21] op_sel_hi:[1,0]
	v_pk_mul_f32 v[144:145], v[144:145], v[20:21] op_sel_hi:[1,0]
	v_pk_mul_f32 v[146:147], v[146:147], v[20:21] op_sel_hi:[1,0]
	v_pk_mul_f32 v[32:33], v[128:129], s[26:27]
	v_pk_mul_f32 v[34:35], v[130:131], s[26:27]
	v_pk_mul_f32 v[36:37], v[144:145], s[26:27]
	v_pk_mul_f32 v[38:39], v[146:147], s[26:27]
	v_pk_fma_f32 v[32:33], v[128:129], v[32:33], s[28:29] neg_lo:[1,0,0] neg_hi:[1,0,0]
	v_pk_fma_f32 v[34:35], v[130:131], v[34:35], s[28:29] neg_lo:[1,0,0] neg_hi:[1,0,0]
	v_pk_fma_f32 v[36:37], v[144:145], v[36:37], s[28:29] neg_lo:[1,0,0] neg_hi:[1,0,0]
	v_pk_fma_f32 v[38:39], v[146:147], v[38:39], s[28:29] neg_lo:[1,0,0] neg_hi:[1,0,0]
	v_pk_mul_f32 v[32:33], v[128:129], v[32:33]
	v_pk_mul_f32 v[34:35], v[130:131], v[34:35]
	v_pk_mul_f32 v[36:37], v[144:145], v[36:37]
	v_pk_mul_f32 v[38:39], v[146:147], v[38:39]
	v_exp_f32_e32 v32, v32
	v_exp_f32_e32 v33, v33
	v_exp_f32_e32 v34, v34
	v_exp_f32_e32 v35, v35
	v_exp_f32_e32 v36, v36
	v_exp_f32_e32 v37, v37
	v_exp_f32_e32 v38, v38
	v_exp_f32_e32 v39, v39
	v_pk_add_f32 v[32:33], v[32:33], s[30:31]
	v_pk_add_f32 v[34:35], v[34:35], s[30:31]
	v_pk_add_f32 v[36:37], v[36:37], s[30:31]
	v_pk_add_f32 v[38:39], v[38:39], s[30:31]
	v_rcp_f32_e32 v32, v32
	v_rcp_f32_e32 v33, v33
	v_rcp_f32_e32 v34, v34
	v_rcp_f32_e32 v35, v35
	v_rcp_f32_e32 v36, v36
	v_rcp_f32_e32 v37, v37
	v_rcp_f32_e32 v38, v38
	v_rcp_f32_e32 v39, v39
	s_nop 0
	v_pk_mul_f32 v[128:129], v[128:129], v[32:33]
	v_pk_mul_f32 v[130:131], v[130:131], v[34:35]
	v_pk_mul_f32 v[144:145], v[144:145], v[36:37]
	v_pk_mul_f32 v[146:147], v[146:147], v[38:39]
	v_cvt_pk_bf16_f32 v64, v128, v129
	v_cvt_pk_bf16_f32 v65, v130, v131
	v_cvt_pk_bf16_f32 v66, v144, v145
	v_cvt_pk_bf16_f32 v67, v146, v147
	global_store_dwordx2 v16, v[64:65], s[10:11]
	global_store_dwordx2 v16, v[66:67], s[10:11] offset:32
	v_pk_mul_f32 v[160:161], v[160:161], v[20:21] op_sel_hi:[1,0]
	v_pk_mul_f32 v[162:163], v[162:163], v[20:21] op_sel_hi:[1,0]
	v_pk_mul_f32 v[176:177], v[176:177], v[20:21] op_sel_hi:[1,0]
	v_pk_mul_f32 v[178:179], v[178:179], v[20:21] op_sel_hi:[1,0]
	v_pk_mul_f32 v[48:49], v[160:161], s[26:27]
	v_pk_mul_f32 v[50:51], v[162:163], s[26:27]
	v_pk_mul_f32 v[52:53], v[176:177], s[26:27]
	v_pk_mul_f32 v[54:55], v[178:179], s[26:27]
	v_pk_fma_f32 v[48:49], v[160:161], v[48:49], s[28:29] neg_lo:[1,0,0] neg_hi:[1,0,0]
	v_pk_fma_f32 v[50:51], v[162:163], v[50:51], s[28:29] neg_lo:[1,0,0] neg_hi:[1,0,0]
	v_pk_fma_f32 v[52:53], v[176:177], v[52:53], s[28:29] neg_lo:[1,0,0] neg_hi:[1,0,0]
	v_pk_fma_f32 v[54:55], v[178:179], v[54:55], s[28:29] neg_lo:[1,0,0] neg_hi:[1,0,0]
	v_pk_mul_f32 v[48:49], v[160:161], v[48:49]
	v_pk_mul_f32 v[50:51], v[162:163], v[50:51]
	v_pk_mul_f32 v[52:53], v[176:177], v[52:53]
	v_pk_mul_f32 v[54:55], v[178:179], v[54:55]
	v_exp_f32_e32 v48, v48
	v_exp_f32_e32 v49, v49
	v_exp_f32_e32 v50, v50
	v_exp_f32_e32 v51, v51
	v_exp_f32_e32 v52, v52
	v_exp_f32_e32 v53, v53
	v_exp_f32_e32 v54, v54
	v_exp_f32_e32 v55, v55
	v_pk_add_f32 v[48:49], v[48:49], s[30:31]
	v_pk_add_f32 v[50:51], v[50:51], s[30:31]
	v_pk_add_f32 v[52:53], v[52:53], s[30:31]
	v_pk_add_f32 v[54:55], v[54:55], s[30:31]
	v_rcp_f32_e32 v48, v48
	v_rcp_f32_e32 v49, v49
	v_rcp_f32_e32 v50, v50
	v_rcp_f32_e32 v51, v51
	v_rcp_f32_e32 v52, v52
	v_rcp_f32_e32 v53, v53
	v_rcp_f32_e32 v54, v54
	v_rcp_f32_e32 v55, v55
	s_nop 0
	v_pk_mul_f32 v[160:161], v[160:161], v[48:49]
	v_pk_mul_f32 v[162:163], v[162:163], v[50:51]
	v_pk_mul_f32 v[176:177], v[176:177], v[52:53]
	v_pk_mul_f32 v[178:179], v[178:179], v[54:55]
	v_cvt_pk_bf16_f32 v68, v160, v161
	v_cvt_pk_bf16_f32 v69, v162, v163
	v_cvt_pk_bf16_f32 v70, v176, v177
	v_cvt_pk_bf16_f32 v71, v178, v179
	global_store_dwordx2 v16, v[68:69], s[10:11] offset:64
	global_store_dwordx2 v16, v[70:71], s[10:11] offset:96
	v_pk_mul_f32 v[192:193], v[192:193], v[20:21] op_sel_hi:[1,0]
	v_pk_mul_f32 v[194:195], v[194:195], v[20:21] op_sel_hi:[1,0]
	v_pk_mul_f32 v[208:209], v[208:209], v[20:21] op_sel_hi:[1,0]
	v_pk_mul_f32 v[210:211], v[210:211], v[20:21] op_sel_hi:[1,0]
	v_pk_mul_f32 v[32:33], v[192:193], s[26:27]
	v_pk_mul_f32 v[34:35], v[194:195], s[26:27]
	v_pk_mul_f32 v[36:37], v[208:209], s[26:27]
	v_pk_mul_f32 v[38:39], v[210:211], s[26:27]
	v_pk_fma_f32 v[32:33], v[192:193], v[32:33], s[28:29] neg_lo:[1,0,0] neg_hi:[1,0,0]
	v_pk_fma_f32 v[34:35], v[194:195], v[34:35], s[28:29] neg_lo:[1,0,0] neg_hi:[1,0,0]
	v_pk_fma_f32 v[36:37], v[208:209], v[36:37], s[28:29] neg_lo:[1,0,0] neg_hi:[1,0,0]
	v_pk_fma_f32 v[38:39], v[210:211], v[38:39], s[28:29] neg_lo:[1,0,0] neg_hi:[1,0,0]
	v_pk_mul_f32 v[32:33], v[192:193], v[32:33]
	v_pk_mul_f32 v[34:35], v[194:195], v[34:35]
	v_pk_mul_f32 v[36:37], v[208:209], v[36:37]
	v_pk_mul_f32 v[38:39], v[210:211], v[38:39]
	v_exp_f32_e32 v32, v32
	v_exp_f32_e32 v33, v33
	v_exp_f32_e32 v34, v34
	v_exp_f32_e32 v35, v35
	v_exp_f32_e32 v36, v36
	v_exp_f32_e32 v37, v37
	v_exp_f32_e32 v38, v38
	v_exp_f32_e32 v39, v39
	v_pk_add_f32 v[32:33], v[32:33], s[30:31]
	v_pk_add_f32 v[34:35], v[34:35], s[30:31]
	v_pk_add_f32 v[36:37], v[36:37], s[30:31]
	v_pk_add_f32 v[38:39], v[38:39], s[30:31]
	v_rcp_f32_e32 v32, v32
	v_rcp_f32_e32 v33, v33
	v_rcp_f32_e32 v34, v34
	v_rcp_f32_e32 v35, v35
	v_rcp_f32_e32 v36, v36
	v_rcp_f32_e32 v37, v37
	v_rcp_f32_e32 v38, v38
	v_rcp_f32_e32 v39, v39
	s_nop 0
	v_pk_mul_f32 v[192:193], v[192:193], v[32:33]
	v_pk_mul_f32 v[194:195], v[194:195], v[34:35]
	v_pk_mul_f32 v[208:209], v[208:209], v[36:37]
	v_pk_mul_f32 v[210:211], v[210:211], v[38:39]
	v_cvt_pk_bf16_f32 v64, v192, v193
	v_cvt_pk_bf16_f32 v65, v194, v195
	v_cvt_pk_bf16_f32 v66, v208, v209
	v_cvt_pk_bf16_f32 v67, v210, v211
	global_store_dwordx2 v16, v[64:65], s[10:11] offset:128
	global_store_dwordx2 v16, v[66:67], s[10:11] offset:160
	v_pk_mul_f32 v[224:225], v[224:225], v[20:21] op_sel_hi:[1,0]
	v_pk_mul_f32 v[226:227], v[226:227], v[20:21] op_sel_hi:[1,0]
	v_pk_mul_f32 v[240:241], v[240:241], v[20:21] op_sel_hi:[1,0]
	v_pk_mul_f32 v[242:243], v[242:243], v[20:21] op_sel_hi:[1,0]
	v_pk_mul_f32 v[48:49], v[224:225], s[26:27]
	v_pk_mul_f32 v[50:51], v[226:227], s[26:27]
	v_pk_mul_f32 v[52:53], v[240:241], s[26:27]
	v_pk_mul_f32 v[54:55], v[242:243], s[26:27]
	v_pk_fma_f32 v[48:49], v[224:225], v[48:49], s[28:29] neg_lo:[1,0,0] neg_hi:[1,0,0]
	v_pk_fma_f32 v[50:51], v[226:227], v[50:51], s[28:29] neg_lo:[1,0,0] neg_hi:[1,0,0]
	v_pk_fma_f32 v[52:53], v[240:241], v[52:53], s[28:29] neg_lo:[1,0,0] neg_hi:[1,0,0]
	v_pk_fma_f32 v[54:55], v[242:243], v[54:55], s[28:29] neg_lo:[1,0,0] neg_hi:[1,0,0]
	v_pk_mul_f32 v[48:49], v[224:225], v[48:49]
	v_pk_mul_f32 v[50:51], v[226:227], v[50:51]
	v_pk_mul_f32 v[52:53], v[240:241], v[52:53]
	v_pk_mul_f32 v[54:55], v[242:243], v[54:55]
	v_exp_f32_e32 v48, v48
	v_exp_f32_e32 v49, v49
	v_exp_f32_e32 v50, v50
	v_exp_f32_e32 v51, v51
	v_exp_f32_e32 v52, v52
	v_exp_f32_e32 v53, v53
	v_exp_f32_e32 v54, v54
	v_exp_f32_e32 v55, v55
	v_pk_add_f32 v[48:49], v[48:49], s[30:31]
	v_pk_add_f32 v[50:51], v[50:51], s[30:31]
	v_pk_add_f32 v[52:53], v[52:53], s[30:31]
	v_pk_add_f32 v[54:55], v[54:55], s[30:31]
	v_rcp_f32_e32 v48, v48
	v_rcp_f32_e32 v49, v49
	v_rcp_f32_e32 v50, v50
	v_rcp_f32_e32 v51, v51
	v_rcp_f32_e32 v52, v52
	v_rcp_f32_e32 v53, v53
	v_rcp_f32_e32 v54, v54
	v_rcp_f32_e32 v55, v55
	s_nop 0
	v_pk_mul_f32 v[224:225], v[224:225], v[48:49]
	v_pk_mul_f32 v[226:227], v[226:227], v[50:51]
	v_pk_mul_f32 v[240:241], v[240:241], v[52:53]
	v_pk_mul_f32 v[242:243], v[242:243], v[54:55]
	v_cvt_pk_bf16_f32 v68, v224, v225
	v_cvt_pk_bf16_f32 v69, v226, v227
	v_cvt_pk_bf16_f32 v70, v240, v241
	v_cvt_pk_bf16_f32 v71, v242, v243
	global_store_dwordx2 v16, v[68:69], s[10:11] offset:192
	global_store_dwordx2 v16, v[70:71], s[10:11] offset:224
	v_pk_mul_f32 v[132:133], v[132:133], v[22:23] op_sel_hi:[1,0]
	v_pk_mul_f32 v[134:135], v[134:135], v[22:23] op_sel_hi:[1,0]
	v_pk_mul_f32 v[148:149], v[148:149], v[22:23] op_sel_hi:[1,0]
	v_pk_mul_f32 v[150:151], v[150:151], v[22:23] op_sel_hi:[1,0]
	v_pk_mul_f32 v[32:33], v[132:133], s[26:27]
	v_pk_mul_f32 v[34:35], v[134:135], s[26:27]
	v_pk_mul_f32 v[36:37], v[148:149], s[26:27]
	v_pk_mul_f32 v[38:39], v[150:151], s[26:27]
	v_pk_fma_f32 v[32:33], v[132:133], v[32:33], s[28:29] neg_lo:[1,0,0] neg_hi:[1,0,0]
	v_pk_fma_f32 v[34:35], v[134:135], v[34:35], s[28:29] neg_lo:[1,0,0] neg_hi:[1,0,0]
	v_pk_fma_f32 v[36:37], v[148:149], v[36:37], s[28:29] neg_lo:[1,0,0] neg_hi:[1,0,0]
	v_pk_fma_f32 v[38:39], v[150:151], v[38:39], s[28:29] neg_lo:[1,0,0] neg_hi:[1,0,0]
	v_pk_mul_f32 v[32:33], v[132:133], v[32:33]
	v_pk_mul_f32 v[34:35], v[134:135], v[34:35]
	v_pk_mul_f32 v[36:37], v[148:149], v[36:37]
	v_pk_mul_f32 v[38:39], v[150:151], v[38:39]
	v_exp_f32_e32 v32, v32
	v_exp_f32_e32 v33, v33
	v_exp_f32_e32 v34, v34
	v_exp_f32_e32 v35, v35
	v_exp_f32_e32 v36, v36
	v_exp_f32_e32 v37, v37
	v_exp_f32_e32 v38, v38
	v_exp_f32_e32 v39, v39
	v_pk_add_f32 v[32:33], v[32:33], s[30:31]
	v_pk_add_f32 v[34:35], v[34:35], s[30:31]
	v_pk_add_f32 v[36:37], v[36:37], s[30:31]
	v_pk_add_f32 v[38:39], v[38:39], s[30:31]
	v_rcp_f32_e32 v32, v32
	v_rcp_f32_e32 v33, v33
	v_rcp_f32_e32 v34, v34
	v_rcp_f32_e32 v35, v35
	v_rcp_f32_e32 v36, v36
	v_rcp_f32_e32 v37, v37
	v_rcp_f32_e32 v38, v38
	v_rcp_f32_e32 v39, v39
	s_nop 0
	v_pk_mul_f32 v[132:133], v[132:133], v[32:33]
	v_pk_mul_f32 v[134:135], v[134:135], v[34:35]
	v_pk_mul_f32 v[148:149], v[148:149], v[36:37]
	v_pk_mul_f32 v[150:151], v[150:151], v[38:39]
	v_cvt_pk_bf16_f32 v64, v132, v133
	v_cvt_pk_bf16_f32 v65, v134, v135
	v_cvt_pk_bf16_f32 v66, v148, v149
	v_cvt_pk_bf16_f32 v67, v150, v151
	global_store_dwordx2 v17, v[64:65], s[10:11]
	global_store_dwordx2 v17, v[66:67], s[10:11] offset:32
	v_pk_mul_f32 v[164:165], v[164:165], v[22:23] op_sel_hi:[1,0]
	v_pk_mul_f32 v[166:167], v[166:167], v[22:23] op_sel_hi:[1,0]
	v_pk_mul_f32 v[180:181], v[180:181], v[22:23] op_sel_hi:[1,0]
	v_pk_mul_f32 v[182:183], v[182:183], v[22:23] op_sel_hi:[1,0]
	v_pk_mul_f32 v[48:49], v[164:165], s[26:27]
	v_pk_mul_f32 v[50:51], v[166:167], s[26:27]
	v_pk_mul_f32 v[52:53], v[180:181], s[26:27]
	v_pk_mul_f32 v[54:55], v[182:183], s[26:27]
	v_pk_fma_f32 v[48:49], v[164:165], v[48:49], s[28:29] neg_lo:[1,0,0] neg_hi:[1,0,0]
	v_pk_fma_f32 v[50:51], v[166:167], v[50:51], s[28:29] neg_lo:[1,0,0] neg_hi:[1,0,0]
	v_pk_fma_f32 v[52:53], v[180:181], v[52:53], s[28:29] neg_lo:[1,0,0] neg_hi:[1,0,0]
	v_pk_fma_f32 v[54:55], v[182:183], v[54:55], s[28:29] neg_lo:[1,0,0] neg_hi:[1,0,0]
	v_pk_mul_f32 v[48:49], v[164:165], v[48:49]
	v_pk_mul_f32 v[50:51], v[166:167], v[50:51]
	v_pk_mul_f32 v[52:53], v[180:181], v[52:53]
	v_pk_mul_f32 v[54:55], v[182:183], v[54:55]
	v_exp_f32_e32 v48, v48
	v_exp_f32_e32 v49, v49
	v_exp_f32_e32 v50, v50
	v_exp_f32_e32 v51, v51
	v_exp_f32_e32 v52, v52
	v_exp_f32_e32 v53, v53
	v_exp_f32_e32 v54, v54
	v_exp_f32_e32 v55, v55
	v_pk_add_f32 v[48:49], v[48:49], s[30:31]
	v_pk_add_f32 v[50:51], v[50:51], s[30:31]
	v_pk_add_f32 v[52:53], v[52:53], s[30:31]
	v_pk_add_f32 v[54:55], v[54:55], s[30:31]
	v_rcp_f32_e32 v48, v48
	v_rcp_f32_e32 v49, v49
	v_rcp_f32_e32 v50, v50
	v_rcp_f32_e32 v51, v51
	v_rcp_f32_e32 v52, v52
	v_rcp_f32_e32 v53, v53
	v_rcp_f32_e32 v54, v54
	v_rcp_f32_e32 v55, v55
	s_nop 0
	v_pk_mul_f32 v[164:165], v[164:165], v[48:49]
	v_pk_mul_f32 v[166:167], v[166:167], v[50:51]
	v_pk_mul_f32 v[180:181], v[180:181], v[52:53]
	v_pk_mul_f32 v[182:183], v[182:183], v[54:55]
	v_cvt_pk_bf16_f32 v68, v164, v165
	v_cvt_pk_bf16_f32 v69, v166, v167
	v_cvt_pk_bf16_f32 v70, v180, v181
	v_cvt_pk_bf16_f32 v71, v182, v183
	global_store_dwordx2 v17, v[68:69], s[10:11] offset:64
	global_store_dwordx2 v17, v[70:71], s[10:11] offset:96
	v_pk_mul_f32 v[196:197], v[196:197], v[22:23] op_sel_hi:[1,0]
	v_pk_mul_f32 v[198:199], v[198:199], v[22:23] op_sel_hi:[1,0]
	v_pk_mul_f32 v[212:213], v[212:213], v[22:23] op_sel_hi:[1,0]
	v_pk_mul_f32 v[214:215], v[214:215], v[22:23] op_sel_hi:[1,0]
	v_pk_mul_f32 v[32:33], v[196:197], s[26:27]
	v_pk_mul_f32 v[34:35], v[198:199], s[26:27]
	v_pk_mul_f32 v[36:37], v[212:213], s[26:27]
	v_pk_mul_f32 v[38:39], v[214:215], s[26:27]
	v_pk_fma_f32 v[32:33], v[196:197], v[32:33], s[28:29] neg_lo:[1,0,0] neg_hi:[1,0,0]
	v_pk_fma_f32 v[34:35], v[198:199], v[34:35], s[28:29] neg_lo:[1,0,0] neg_hi:[1,0,0]
	v_pk_fma_f32 v[36:37], v[212:213], v[36:37], s[28:29] neg_lo:[1,0,0] neg_hi:[1,0,0]
	v_pk_fma_f32 v[38:39], v[214:215], v[38:39], s[28:29] neg_lo:[1,0,0] neg_hi:[1,0,0]
	v_pk_mul_f32 v[32:33], v[196:197], v[32:33]
	v_pk_mul_f32 v[34:35], v[198:199], v[34:35]
	v_pk_mul_f32 v[36:37], v[212:213], v[36:37]
	v_pk_mul_f32 v[38:39], v[214:215], v[38:39]
	v_exp_f32_e32 v32, v32
	v_exp_f32_e32 v33, v33
	v_exp_f32_e32 v34, v34
	v_exp_f32_e32 v35, v35
	v_exp_f32_e32 v36, v36
	v_exp_f32_e32 v37, v37
	v_exp_f32_e32 v38, v38
	v_exp_f32_e32 v39, v39
	v_pk_add_f32 v[32:33], v[32:33], s[30:31]
	v_pk_add_f32 v[34:35], v[34:35], s[30:31]
	v_pk_add_f32 v[36:37], v[36:37], s[30:31]
	v_pk_add_f32 v[38:39], v[38:39], s[30:31]
	v_rcp_f32_e32 v32, v32
	v_rcp_f32_e32 v33, v33
	v_rcp_f32_e32 v34, v34
	v_rcp_f32_e32 v35, v35
	v_rcp_f32_e32 v36, v36
	v_rcp_f32_e32 v37, v37
	v_rcp_f32_e32 v38, v38
	v_rcp_f32_e32 v39, v39
	s_nop 0
	v_pk_mul_f32 v[196:197], v[196:197], v[32:33]
	v_pk_mul_f32 v[198:199], v[198:199], v[34:35]
	v_pk_mul_f32 v[212:213], v[212:213], v[36:37]
	v_pk_mul_f32 v[214:215], v[214:215], v[38:39]
	v_cvt_pk_bf16_f32 v64, v196, v197
	v_cvt_pk_bf16_f32 v65, v198, v199
	v_cvt_pk_bf16_f32 v66, v212, v213
	v_cvt_pk_bf16_f32 v67, v214, v215
	global_store_dwordx2 v17, v[64:65], s[10:11] offset:128
	global_store_dwordx2 v17, v[66:67], s[10:11] offset:160
	v_pk_mul_f32 v[228:229], v[228:229], v[22:23] op_sel_hi:[1,0]
	v_pk_mul_f32 v[230:231], v[230:231], v[22:23] op_sel_hi:[1,0]
	v_pk_mul_f32 v[244:245], v[244:245], v[22:23] op_sel_hi:[1,0]
	v_pk_mul_f32 v[246:247], v[246:247], v[22:23] op_sel_hi:[1,0]
	v_pk_mul_f32 v[48:49], v[228:229], s[26:27]
	v_pk_mul_f32 v[50:51], v[230:231], s[26:27]
	v_pk_mul_f32 v[52:53], v[244:245], s[26:27]
	v_pk_mul_f32 v[54:55], v[246:247], s[26:27]
	v_pk_fma_f32 v[48:49], v[228:229], v[48:49], s[28:29] neg_lo:[1,0,0] neg_hi:[1,0,0]
	v_pk_fma_f32 v[50:51], v[230:231], v[50:51], s[28:29] neg_lo:[1,0,0] neg_hi:[1,0,0]
	v_pk_fma_f32 v[52:53], v[244:245], v[52:53], s[28:29] neg_lo:[1,0,0] neg_hi:[1,0,0]
	v_pk_fma_f32 v[54:55], v[246:247], v[54:55], s[28:29] neg_lo:[1,0,0] neg_hi:[1,0,0]
	v_pk_mul_f32 v[48:49], v[228:229], v[48:49]
	v_pk_mul_f32 v[50:51], v[230:231], v[50:51]
	v_pk_mul_f32 v[52:53], v[244:245], v[52:53]
	v_pk_mul_f32 v[54:55], v[246:247], v[54:55]
	v_exp_f32_e32 v48, v48
	v_exp_f32_e32 v49, v49
	v_exp_f32_e32 v50, v50
	v_exp_f32_e32 v51, v51
	v_exp_f32_e32 v52, v52
	v_exp_f32_e32 v53, v53
	v_exp_f32_e32 v54, v54
	v_exp_f32_e32 v55, v55
	v_pk_add_f32 v[48:49], v[48:49], s[30:31]
	v_pk_add_f32 v[50:51], v[50:51], s[30:31]
	v_pk_add_f32 v[52:53], v[52:53], s[30:31]
	v_pk_add_f32 v[54:55], v[54:55], s[30:31]
	v_rcp_f32_e32 v48, v48
	v_rcp_f32_e32 v49, v49
	v_rcp_f32_e32 v50, v50
	v_rcp_f32_e32 v51, v51
	v_rcp_f32_e32 v52, v52
	v_rcp_f32_e32 v53, v53
	v_rcp_f32_e32 v54, v54
	v_rcp_f32_e32 v55, v55
	s_nop 0
	v_pk_mul_f32 v[228:229], v[228:229], v[48:49]
	v_pk_mul_f32 v[230:231], v[230:231], v[50:51]
	v_pk_mul_f32 v[244:245], v[244:245], v[52:53]
	v_pk_mul_f32 v[246:247], v[246:247], v[54:55]
	v_cvt_pk_bf16_f32 v68, v228, v229
	v_cvt_pk_bf16_f32 v69, v230, v231
	v_cvt_pk_bf16_f32 v70, v244, v245
	v_cvt_pk_bf16_f32 v71, v246, v247
	global_store_dwordx2 v17, v[68:69], s[10:11] offset:192
	global_store_dwordx2 v17, v[70:71], s[10:11] offset:224
	v_pk_mul_f32 v[136:137], v[136:137], v[24:25] op_sel_hi:[1,0]
	v_pk_mul_f32 v[138:139], v[138:139], v[24:25] op_sel_hi:[1,0]
	v_pk_mul_f32 v[152:153], v[152:153], v[24:25] op_sel_hi:[1,0]
	v_pk_mul_f32 v[154:155], v[154:155], v[24:25] op_sel_hi:[1,0]
	v_pk_mul_f32 v[32:33], v[136:137], s[26:27]
	v_pk_mul_f32 v[34:35], v[138:139], s[26:27]
	v_pk_mul_f32 v[36:37], v[152:153], s[26:27]
	v_pk_mul_f32 v[38:39], v[154:155], s[26:27]
	v_pk_fma_f32 v[32:33], v[136:137], v[32:33], s[28:29] neg_lo:[1,0,0] neg_hi:[1,0,0]
	v_pk_fma_f32 v[34:35], v[138:139], v[34:35], s[28:29] neg_lo:[1,0,0] neg_hi:[1,0,0]
	v_pk_fma_f32 v[36:37], v[152:153], v[36:37], s[28:29] neg_lo:[1,0,0] neg_hi:[1,0,0]
	v_pk_fma_f32 v[38:39], v[154:155], v[38:39], s[28:29] neg_lo:[1,0,0] neg_hi:[1,0,0]
	v_pk_mul_f32 v[32:33], v[136:137], v[32:33]
	v_pk_mul_f32 v[34:35], v[138:139], v[34:35]
	v_pk_mul_f32 v[36:37], v[152:153], v[36:37]
	v_pk_mul_f32 v[38:39], v[154:155], v[38:39]
	v_exp_f32_e32 v32, v32
	v_exp_f32_e32 v33, v33
	v_exp_f32_e32 v34, v34
	v_exp_f32_e32 v35, v35
	v_exp_f32_e32 v36, v36
	v_exp_f32_e32 v37, v37
	v_exp_f32_e32 v38, v38
	v_exp_f32_e32 v39, v39
	v_pk_add_f32 v[32:33], v[32:33], s[30:31]
	v_pk_add_f32 v[34:35], v[34:35], s[30:31]
	v_pk_add_f32 v[36:37], v[36:37], s[30:31]
	v_pk_add_f32 v[38:39], v[38:39], s[30:31]
	v_rcp_f32_e32 v32, v32
	v_rcp_f32_e32 v33, v33
	v_rcp_f32_e32 v34, v34
	v_rcp_f32_e32 v35, v35
	v_rcp_f32_e32 v36, v36
	v_rcp_f32_e32 v37, v37
	v_rcp_f32_e32 v38, v38
	v_rcp_f32_e32 v39, v39
	s_nop 0
	v_pk_mul_f32 v[136:137], v[136:137], v[32:33]
	v_pk_mul_f32 v[138:139], v[138:139], v[34:35]
	v_pk_mul_f32 v[152:153], v[152:153], v[36:37]
	v_pk_mul_f32 v[154:155], v[154:155], v[38:39]
	v_cvt_pk_bf16_f32 v64, v136, v137
	v_cvt_pk_bf16_f32 v65, v138, v139
	v_cvt_pk_bf16_f32 v66, v152, v153
	v_cvt_pk_bf16_f32 v67, v154, v155
	global_store_dwordx2 v18, v[64:65], s[10:11]
	global_store_dwordx2 v18, v[66:67], s[10:11] offset:32
	v_pk_mul_f32 v[168:169], v[168:169], v[24:25] op_sel_hi:[1,0]
	v_pk_mul_f32 v[170:171], v[170:171], v[24:25] op_sel_hi:[1,0]
	v_pk_mul_f32 v[184:185], v[184:185], v[24:25] op_sel_hi:[1,0]
	v_pk_mul_f32 v[186:187], v[186:187], v[24:25] op_sel_hi:[1,0]
	v_pk_mul_f32 v[48:49], v[168:169], s[26:27]
	v_pk_mul_f32 v[50:51], v[170:171], s[26:27]
	v_pk_mul_f32 v[52:53], v[184:185], s[26:27]
	v_pk_mul_f32 v[54:55], v[186:187], s[26:27]
	v_pk_fma_f32 v[48:49], v[168:169], v[48:49], s[28:29] neg_lo:[1,0,0] neg_hi:[1,0,0]
	v_pk_fma_f32 v[50:51], v[170:171], v[50:51], s[28:29] neg_lo:[1,0,0] neg_hi:[1,0,0]
	v_pk_fma_f32 v[52:53], v[184:185], v[52:53], s[28:29] neg_lo:[1,0,0] neg_hi:[1,0,0]
	v_pk_fma_f32 v[54:55], v[186:187], v[54:55], s[28:29] neg_lo:[1,0,0] neg_hi:[1,0,0]
	v_pk_mul_f32 v[48:49], v[168:169], v[48:49]
	v_pk_mul_f32 v[50:51], v[170:171], v[50:51]
	v_pk_mul_f32 v[52:53], v[184:185], v[52:53]
	v_pk_mul_f32 v[54:55], v[186:187], v[54:55]
	v_exp_f32_e32 v48, v48
	v_exp_f32_e32 v49, v49
	v_exp_f32_e32 v50, v50
	v_exp_f32_e32 v51, v51
	v_exp_f32_e32 v52, v52
	v_exp_f32_e32 v53, v53
	v_exp_f32_e32 v54, v54
	v_exp_f32_e32 v55, v55
	v_pk_add_f32 v[48:49], v[48:49], s[30:31]
	v_pk_add_f32 v[50:51], v[50:51], s[30:31]
	v_pk_add_f32 v[52:53], v[52:53], s[30:31]
	v_pk_add_f32 v[54:55], v[54:55], s[30:31]
	v_rcp_f32_e32 v48, v48
	v_rcp_f32_e32 v49, v49
	v_rcp_f32_e32 v50, v50
	v_rcp_f32_e32 v51, v51
	v_rcp_f32_e32 v52, v52
	v_rcp_f32_e32 v53, v53
	v_rcp_f32_e32 v54, v54
	v_rcp_f32_e32 v55, v55
	s_nop 0
	v_pk_mul_f32 v[168:169], v[168:169], v[48:49]
	v_pk_mul_f32 v[170:171], v[170:171], v[50:51]
	v_pk_mul_f32 v[184:185], v[184:185], v[52:53]
	v_pk_mul_f32 v[186:187], v[186:187], v[54:55]
	v_cvt_pk_bf16_f32 v68, v168, v169
	v_cvt_pk_bf16_f32 v69, v170, v171
	v_cvt_pk_bf16_f32 v70, v184, v185
	v_cvt_pk_bf16_f32 v71, v186, v187
	global_store_dwordx2 v18, v[68:69], s[10:11] offset:64
	global_store_dwordx2 v18, v[70:71], s[10:11] offset:96
	v_pk_mul_f32 v[200:201], v[200:201], v[24:25] op_sel_hi:[1,0]
	v_pk_mul_f32 v[202:203], v[202:203], v[24:25] op_sel_hi:[1,0]
	v_pk_mul_f32 v[216:217], v[216:217], v[24:25] op_sel_hi:[1,0]
	v_pk_mul_f32 v[218:219], v[218:219], v[24:25] op_sel_hi:[1,0]
	v_pk_mul_f32 v[32:33], v[200:201], s[26:27]
	v_pk_mul_f32 v[34:35], v[202:203], s[26:27]
	v_pk_mul_f32 v[36:37], v[216:217], s[26:27]
	v_pk_mul_f32 v[38:39], v[218:219], s[26:27]
	v_pk_fma_f32 v[32:33], v[200:201], v[32:33], s[28:29] neg_lo:[1,0,0] neg_hi:[1,0,0]
	v_pk_fma_f32 v[34:35], v[202:203], v[34:35], s[28:29] neg_lo:[1,0,0] neg_hi:[1,0,0]
	v_pk_fma_f32 v[36:37], v[216:217], v[36:37], s[28:29] neg_lo:[1,0,0] neg_hi:[1,0,0]
	v_pk_fma_f32 v[38:39], v[218:219], v[38:39], s[28:29] neg_lo:[1,0,0] neg_hi:[1,0,0]
	v_pk_mul_f32 v[32:33], v[200:201], v[32:33]
	v_pk_mul_f32 v[34:35], v[202:203], v[34:35]
	v_pk_mul_f32 v[36:37], v[216:217], v[36:37]
	v_pk_mul_f32 v[38:39], v[218:219], v[38:39]
	v_exp_f32_e32 v32, v32
	v_exp_f32_e32 v33, v33
	v_exp_f32_e32 v34, v34
	v_exp_f32_e32 v35, v35
	v_exp_f32_e32 v36, v36
	v_exp_f32_e32 v37, v37
	v_exp_f32_e32 v38, v38
	v_exp_f32_e32 v39, v39
	v_pk_add_f32 v[32:33], v[32:33], s[30:31]
	v_pk_add_f32 v[34:35], v[34:35], s[30:31]
	v_pk_add_f32 v[36:37], v[36:37], s[30:31]
	v_pk_add_f32 v[38:39], v[38:39], s[30:31]
	v_rcp_f32_e32 v32, v32
	v_rcp_f32_e32 v33, v33
	v_rcp_f32_e32 v34, v34
	v_rcp_f32_e32 v35, v35
	v_rcp_f32_e32 v36, v36
	v_rcp_f32_e32 v37, v37
	v_rcp_f32_e32 v38, v38
	v_rcp_f32_e32 v39, v39
	s_nop 0
	v_pk_mul_f32 v[200:201], v[200:201], v[32:33]
	v_pk_mul_f32 v[202:203], v[202:203], v[34:35]
	v_pk_mul_f32 v[216:217], v[216:217], v[36:37]
	v_pk_mul_f32 v[218:219], v[218:219], v[38:39]
	v_cvt_pk_bf16_f32 v64, v200, v201
	v_cvt_pk_bf16_f32 v65, v202, v203
	v_cvt_pk_bf16_f32 v66, v216, v217
	v_cvt_pk_bf16_f32 v67, v218, v219
	global_store_dwordx2 v18, v[64:65], s[10:11] offset:128
	global_store_dwordx2 v18, v[66:67], s[10:11] offset:160
	v_pk_mul_f32 v[232:233], v[232:233], v[24:25] op_sel_hi:[1,0]
	v_pk_mul_f32 v[234:235], v[234:235], v[24:25] op_sel_hi:[1,0]
	v_pk_mul_f32 v[248:249], v[248:249], v[24:25] op_sel_hi:[1,0]
	v_pk_mul_f32 v[250:251], v[250:251], v[24:25] op_sel_hi:[1,0]
	v_pk_mul_f32 v[48:49], v[232:233], s[26:27]
	v_pk_mul_f32 v[50:51], v[234:235], s[26:27]
	v_pk_mul_f32 v[52:53], v[248:249], s[26:27]
	v_pk_mul_f32 v[54:55], v[250:251], s[26:27]
	v_pk_fma_f32 v[48:49], v[232:233], v[48:49], s[28:29] neg_lo:[1,0,0] neg_hi:[1,0,0]
	v_pk_fma_f32 v[50:51], v[234:235], v[50:51], s[28:29] neg_lo:[1,0,0] neg_hi:[1,0,0]
	v_pk_fma_f32 v[52:53], v[248:249], v[52:53], s[28:29] neg_lo:[1,0,0] neg_hi:[1,0,0]
	v_pk_fma_f32 v[54:55], v[250:251], v[54:55], s[28:29] neg_lo:[1,0,0] neg_hi:[1,0,0]
	v_pk_mul_f32 v[48:49], v[232:233], v[48:49]
	v_pk_mul_f32 v[50:51], v[234:235], v[50:51]
	v_pk_mul_f32 v[52:53], v[248:249], v[52:53]
	v_pk_mul_f32 v[54:55], v[250:251], v[54:55]
	v_exp_f32_e32 v48, v48
	v_exp_f32_e32 v49, v49
	v_exp_f32_e32 v50, v50
	v_exp_f32_e32 v51, v51
	v_exp_f32_e32 v52, v52
	v_exp_f32_e32 v53, v53
	v_exp_f32_e32 v54, v54
	v_exp_f32_e32 v55, v55
	v_pk_add_f32 v[48:49], v[48:49], s[30:31]
	v_pk_add_f32 v[50:51], v[50:51], s[30:31]
	v_pk_add_f32 v[52:53], v[52:53], s[30:31]
	v_pk_add_f32 v[54:55], v[54:55], s[30:31]
	v_rcp_f32_e32 v48, v48
	v_rcp_f32_e32 v49, v49
	v_rcp_f32_e32 v50, v50
	v_rcp_f32_e32 v51, v51
	v_rcp_f32_e32 v52, v52
	v_rcp_f32_e32 v53, v53
	v_rcp_f32_e32 v54, v54
	v_rcp_f32_e32 v55, v55
	s_nop 0
	v_pk_mul_f32 v[232:233], v[232:233], v[48:49]
	v_pk_mul_f32 v[234:235], v[234:235], v[50:51]
	v_pk_mul_f32 v[248:249], v[248:249], v[52:53]
	v_pk_mul_f32 v[250:251], v[250:251], v[54:55]
	v_cvt_pk_bf16_f32 v68, v232, v233
	v_cvt_pk_bf16_f32 v69, v234, v235
	v_cvt_pk_bf16_f32 v70, v248, v249
	v_cvt_pk_bf16_f32 v71, v250, v251
	global_store_dwordx2 v18, v[68:69], s[10:11] offset:192
	global_store_dwordx2 v18, v[70:71], s[10:11] offset:224
	v_pk_mul_f32 v[140:141], v[140:141], v[26:27] op_sel_hi:[1,0]
	v_pk_mul_f32 v[142:143], v[142:143], v[26:27] op_sel_hi:[1,0]
	v_pk_mul_f32 v[156:157], v[156:157], v[26:27] op_sel_hi:[1,0]
	v_pk_mul_f32 v[158:159], v[158:159], v[26:27] op_sel_hi:[1,0]
	v_pk_mul_f32 v[32:33], v[140:141], s[26:27]
	v_pk_mul_f32 v[34:35], v[142:143], s[26:27]
	v_pk_mul_f32 v[36:37], v[156:157], s[26:27]
	v_pk_mul_f32 v[38:39], v[158:159], s[26:27]
	v_pk_fma_f32 v[32:33], v[140:141], v[32:33], s[28:29] neg_lo:[1,0,0] neg_hi:[1,0,0]
	v_pk_fma_f32 v[34:35], v[142:143], v[34:35], s[28:29] neg_lo:[1,0,0] neg_hi:[1,0,0]
	v_pk_fma_f32 v[36:37], v[156:157], v[36:37], s[28:29] neg_lo:[1,0,0] neg_hi:[1,0,0]
	v_pk_fma_f32 v[38:39], v[158:159], v[38:39], s[28:29] neg_lo:[1,0,0] neg_hi:[1,0,0]
	v_pk_mul_f32 v[32:33], v[140:141], v[32:33]
	v_pk_mul_f32 v[34:35], v[142:143], v[34:35]
	v_pk_mul_f32 v[36:37], v[156:157], v[36:37]
	v_pk_mul_f32 v[38:39], v[158:159], v[38:39]
	v_exp_f32_e32 v32, v32
	v_exp_f32_e32 v33, v33
	v_exp_f32_e32 v34, v34
	v_exp_f32_e32 v35, v35
	v_exp_f32_e32 v36, v36
	v_exp_f32_e32 v37, v37
	v_exp_f32_e32 v38, v38
	v_exp_f32_e32 v39, v39
	v_pk_add_f32 v[32:33], v[32:33], s[30:31]
	v_pk_add_f32 v[34:35], v[34:35], s[30:31]
	v_pk_add_f32 v[36:37], v[36:37], s[30:31]
	v_pk_add_f32 v[38:39], v[38:39], s[30:31]
	v_rcp_f32_e32 v32, v32
	v_rcp_f32_e32 v33, v33
	v_rcp_f32_e32 v34, v34
	v_rcp_f32_e32 v35, v35
	v_rcp_f32_e32 v36, v36
	v_rcp_f32_e32 v37, v37
	v_rcp_f32_e32 v38, v38
	v_rcp_f32_e32 v39, v39
	s_nop 0
	v_pk_mul_f32 v[140:141], v[140:141], v[32:33]
	v_pk_mul_f32 v[142:143], v[142:143], v[34:35]
	v_pk_mul_f32 v[156:157], v[156:157], v[36:37]
	v_pk_mul_f32 v[158:159], v[158:159], v[38:39]
	v_cvt_pk_bf16_f32 v64, v140, v141
	v_cvt_pk_bf16_f32 v65, v142, v143
	v_cvt_pk_bf16_f32 v66, v156, v157
	v_cvt_pk_bf16_f32 v67, v158, v159
	global_store_dwordx2 v19, v[64:65], s[10:11]
	global_store_dwordx2 v19, v[66:67], s[10:11] offset:32
	v_pk_mul_f32 v[172:173], v[172:173], v[26:27] op_sel_hi:[1,0]
	v_pk_mul_f32 v[174:175], v[174:175], v[26:27] op_sel_hi:[1,0]
	v_pk_mul_f32 v[188:189], v[188:189], v[26:27] op_sel_hi:[1,0]
	v_pk_mul_f32 v[190:191], v[190:191], v[26:27] op_sel_hi:[1,0]
	v_pk_mul_f32 v[48:49], v[172:173], s[26:27]
	v_pk_mul_f32 v[50:51], v[174:175], s[26:27]
	v_pk_mul_f32 v[52:53], v[188:189], s[26:27]
	v_pk_mul_f32 v[54:55], v[190:191], s[26:27]
	v_pk_fma_f32 v[48:49], v[172:173], v[48:49], s[28:29] neg_lo:[1,0,0] neg_hi:[1,0,0]
	v_pk_fma_f32 v[50:51], v[174:175], v[50:51], s[28:29] neg_lo:[1,0,0] neg_hi:[1,0,0]
	v_pk_fma_f32 v[52:53], v[188:189], v[52:53], s[28:29] neg_lo:[1,0,0] neg_hi:[1,0,0]
	v_pk_fma_f32 v[54:55], v[190:191], v[54:55], s[28:29] neg_lo:[1,0,0] neg_hi:[1,0,0]
	v_pk_mul_f32 v[48:49], v[172:173], v[48:49]
	v_pk_mul_f32 v[50:51], v[174:175], v[50:51]
	v_pk_mul_f32 v[52:53], v[188:189], v[52:53]
	v_pk_mul_f32 v[54:55], v[190:191], v[54:55]
	v_exp_f32_e32 v48, v48
	v_exp_f32_e32 v49, v49
	v_exp_f32_e32 v50, v50
	v_exp_f32_e32 v51, v51
	v_exp_f32_e32 v52, v52
	v_exp_f32_e32 v53, v53
	v_exp_f32_e32 v54, v54
	v_exp_f32_e32 v55, v55
	v_pk_add_f32 v[48:49], v[48:49], s[30:31]
	v_pk_add_f32 v[50:51], v[50:51], s[30:31]
	v_pk_add_f32 v[52:53], v[52:53], s[30:31]
	v_pk_add_f32 v[54:55], v[54:55], s[30:31]
	v_rcp_f32_e32 v48, v48
	v_rcp_f32_e32 v49, v49
	v_rcp_f32_e32 v50, v50
	v_rcp_f32_e32 v51, v51
	v_rcp_f32_e32 v52, v52
	v_rcp_f32_e32 v53, v53
	v_rcp_f32_e32 v54, v54
	v_rcp_f32_e32 v55, v55
	s_nop 0
	v_pk_mul_f32 v[172:173], v[172:173], v[48:49]
	v_pk_mul_f32 v[174:175], v[174:175], v[50:51]
	v_pk_mul_f32 v[188:189], v[188:189], v[52:53]
	v_pk_mul_f32 v[190:191], v[190:191], v[54:55]
	v_cvt_pk_bf16_f32 v68, v172, v173
	v_cvt_pk_bf16_f32 v69, v174, v175
	v_cvt_pk_bf16_f32 v70, v188, v189
	v_cvt_pk_bf16_f32 v71, v190, v191
	global_store_dwordx2 v19, v[68:69], s[10:11] offset:64
	global_store_dwordx2 v19, v[70:71], s[10:11] offset:96
	v_pk_mul_f32 v[204:205], v[204:205], v[26:27] op_sel_hi:[1,0]
	v_pk_mul_f32 v[206:207], v[206:207], v[26:27] op_sel_hi:[1,0]
	v_pk_mul_f32 v[220:221], v[220:221], v[26:27] op_sel_hi:[1,0]
	v_pk_mul_f32 v[222:223], v[222:223], v[26:27] op_sel_hi:[1,0]
	v_pk_mul_f32 v[32:33], v[204:205], s[26:27]
	v_pk_mul_f32 v[34:35], v[206:207], s[26:27]
	v_pk_mul_f32 v[36:37], v[220:221], s[26:27]
	v_pk_mul_f32 v[38:39], v[222:223], s[26:27]
	v_pk_fma_f32 v[32:33], v[204:205], v[32:33], s[28:29] neg_lo:[1,0,0] neg_hi:[1,0,0]
	v_pk_fma_f32 v[34:35], v[206:207], v[34:35], s[28:29] neg_lo:[1,0,0] neg_hi:[1,0,0]
	v_pk_fma_f32 v[36:37], v[220:221], v[36:37], s[28:29] neg_lo:[1,0,0] neg_hi:[1,0,0]
	v_pk_fma_f32 v[38:39], v[222:223], v[38:39], s[28:29] neg_lo:[1,0,0] neg_hi:[1,0,0]
	v_pk_mul_f32 v[32:33], v[204:205], v[32:33]
	v_pk_mul_f32 v[34:35], v[206:207], v[34:35]
	v_pk_mul_f32 v[36:37], v[220:221], v[36:37]
	v_pk_mul_f32 v[38:39], v[222:223], v[38:39]
	v_exp_f32_e32 v32, v32
	v_exp_f32_e32 v33, v33
	v_exp_f32_e32 v34, v34
	v_exp_f32_e32 v35, v35
	v_exp_f32_e32 v36, v36
	v_exp_f32_e32 v37, v37
	v_exp_f32_e32 v38, v38
	v_exp_f32_e32 v39, v39
	v_pk_add_f32 v[32:33], v[32:33], s[30:31]
	v_pk_add_f32 v[34:35], v[34:35], s[30:31]
	v_pk_add_f32 v[36:37], v[36:37], s[30:31]
	v_pk_add_f32 v[38:39], v[38:39], s[30:31]
	v_rcp_f32_e32 v32, v32
	v_rcp_f32_e32 v33, v33
	v_rcp_f32_e32 v34, v34
	v_rcp_f32_e32 v35, v35
	v_rcp_f32_e32 v36, v36
	v_rcp_f32_e32 v37, v37
	v_rcp_f32_e32 v38, v38
	v_rcp_f32_e32 v39, v39
	s_nop 0
	v_pk_mul_f32 v[204:205], v[204:205], v[32:33]
	v_pk_mul_f32 v[206:207], v[206:207], v[34:35]
	v_pk_mul_f32 v[220:221], v[220:221], v[36:37]
	v_pk_mul_f32 v[222:223], v[222:223], v[38:39]
	v_cvt_pk_bf16_f32 v64, v204, v205
	v_cvt_pk_bf16_f32 v65, v206, v207
	v_cvt_pk_bf16_f32 v66, v220, v221
	v_cvt_pk_bf16_f32 v67, v222, v223
	global_store_dwordx2 v19, v[64:65], s[10:11] offset:128
	global_store_dwordx2 v19, v[66:67], s[10:11] offset:160
	v_pk_mul_f32 v[236:237], v[236:237], v[26:27] op_sel_hi:[1,0]
	v_pk_mul_f32 v[238:239], v[238:239], v[26:27] op_sel_hi:[1,0]
	v_pk_mul_f32 v[252:253], v[252:253], v[26:27] op_sel_hi:[1,0]
	v_pk_mul_f32 v[254:255], v[254:255], v[26:27] op_sel_hi:[1,0]
	v_pk_mul_f32 v[48:49], v[236:237], s[26:27]
	v_pk_mul_f32 v[50:51], v[238:239], s[26:27]
	v_pk_mul_f32 v[52:53], v[252:253], s[26:27]
	v_pk_mul_f32 v[54:55], v[254:255], s[26:27]
	v_pk_fma_f32 v[48:49], v[236:237], v[48:49], s[28:29] neg_lo:[1,0,0] neg_hi:[1,0,0]
	v_pk_fma_f32 v[50:51], v[238:239], v[50:51], s[28:29] neg_lo:[1,0,0] neg_hi:[1,0,0]
	v_pk_fma_f32 v[52:53], v[252:253], v[52:53], s[28:29] neg_lo:[1,0,0] neg_hi:[1,0,0]
	v_pk_fma_f32 v[54:55], v[254:255], v[54:55], s[28:29] neg_lo:[1,0,0] neg_hi:[1,0,0]
	v_pk_mul_f32 v[48:49], v[236:237], v[48:49]
	v_pk_mul_f32 v[50:51], v[238:239], v[50:51]
	v_pk_mul_f32 v[52:53], v[252:253], v[52:53]
	v_pk_mul_f32 v[54:55], v[254:255], v[54:55]
	v_exp_f32_e32 v48, v48
	v_exp_f32_e32 v49, v49
	v_exp_f32_e32 v50, v50
	v_exp_f32_e32 v51, v51
	v_exp_f32_e32 v52, v52
	v_exp_f32_e32 v53, v53
	v_exp_f32_e32 v54, v54
	v_exp_f32_e32 v55, v55
	v_pk_add_f32 v[48:49], v[48:49], s[30:31]
	v_pk_add_f32 v[50:51], v[50:51], s[30:31]
	v_pk_add_f32 v[52:53], v[52:53], s[30:31]
	v_pk_add_f32 v[54:55], v[54:55], s[30:31]
	v_rcp_f32_e32 v48, v48
	v_rcp_f32_e32 v49, v49
	v_rcp_f32_e32 v50, v50
	v_rcp_f32_e32 v51, v51
	v_rcp_f32_e32 v52, v52
	v_rcp_f32_e32 v53, v53
	v_rcp_f32_e32 v54, v54
	v_rcp_f32_e32 v55, v55
	s_nop 0
	v_pk_mul_f32 v[236:237], v[236:237], v[48:49]
	v_pk_mul_f32 v[238:239], v[238:239], v[50:51]
	v_pk_mul_f32 v[252:253], v[252:253], v[52:53]
	v_pk_mul_f32 v[254:255], v[254:255], v[54:55]
	v_cvt_pk_bf16_f32 v68, v236, v237
	v_cvt_pk_bf16_f32 v69, v238, v239
	v_cvt_pk_bf16_f32 v70, v252, v253
	v_cvt_pk_bf16_f32 v71, v254, v255
	global_store_dwordx2 v19, v[68:69], s[10:11] offset:192
	global_store_dwordx2 v19, v[70:71], s[10:11] offset:224
